# v57 plus nt hint on the full-row stores of the row-wise phases (normalised rows, latent rows, MLA keys, gathered slot rows)
# speedup vs baseline: 1.0008x; 1.0008x over previous
.LBB0_53:
	v_mul_f32_e32 v58, v55, v55
	v_mul_f32_e32 v59, v53, v53
	v_fmac_f32_e32 v58, v54, v54
	v_fmac_f32_e32 v59, v52, v52
	v_add_f32_e32 v58, v58, v59
	v_mul_f32_e32 v59, v51, v51
	v_mul_f32_e32 v60, v49, v49
	v_fmac_f32_e32 v59, v50, v50
	v_fmac_f32_e32 v60, v48, v48
	v_add_f32_e32 v59, v59, v60
	v_add_f32_e32 v58, v58, v59
	v_mul_f32_e32 v59, v47, v47
	v_mul_f32_e32 v60, v43, v43
	v_fmac_f32_e32 v59, v46, v46
	v_fmac_f32_e32 v60, v42, v42
	v_add_f32_e32 v59, v59, v60
	v_add_f32_e32 v58, v59, v58
	v_mul_f32_e32 v59, v45, v45
	v_mul_f32_e32 v60, v41, v41
	v_fmac_f32_e32 v59, v44, v44
	v_fmac_f32_e32 v60, v40, v40
	v_add_f32_e32 v59, v59, v60
	v_add_f32_e32 v58, v59, v58
	v_add_co_u32_e32 v56, vcc, s10, v56
	s_nop 0
	v_add_f32_dpp v58, v58, v58 quad_perm:[1,0,3,2] row_mask:0xf bank_mask:0xf bound_ctrl:1
	v_addc_co_u32_e32 v57, vcc, 0, v57, vcc
	s_nop 0
	v_add_f32_dpp v58, v58, v58 quad_perm:[2,3,0,1] row_mask:0xf bank_mask:0xf bound_ctrl:1
	s_addk_i32 s6, 0x800
	v_lshl_add_u64 v[36:37], v[36:37], 0, s[22:23]
	v_add_f32_dpp v58, v58, v58 row_half_mirror row_mask:0xf bank_mask:0xf bound_ctrl:1
	s_nop 1
	v_add_f32_dpp v58, v58, v58 row_mirror row_mask:0xf bank_mask:0xf bound_ctrl:1
	v_mov_b32_e32 v59, v58
	s_nop 1
	v_permlane16_swap_b32_e32 v58, v59
	v_add_f32_e32 v58, v58, v59
	v_mov_b32_e32 v59, v58
	s_nop 1
	v_permlane32_swap_b32_e32 v58, v59
	v_add_f32_e32 v58, v58, v59
	v_fmamk_f32 v58, v58, 0x3a800000, v240
	v_rsq_f32_e32 v58, v58
	s_nop 0
	v_pk_mul_f32 v[60:61], v[54:55], v[58:59] op_sel_hi:[1,0]
	v_pk_mul_f32 v[62:63], v[52:53], v[58:59] op_sel_hi:[1,0]
	s_waitcnt vmcnt(1)
	v_pk_mul_f32 v[60:61], v[8:9], v[60:61]
	v_pk_mul_f32 v[62:63], v[10:11], v[62:63]
	v_cvt_pk_bf16_f32 v60, v60, v61
	v_cvt_pk_bf16_f32 v61, v62, v63
	global_store_dwordx2 v[56:57], v[60:61], off nt
	v_pk_mul_f32 v[60:61], v[50:51], v[58:59] op_sel_hi:[1,0]
	v_pk_mul_f32 v[62:63], v[48:49], v[58:59] op_sel_hi:[1,0]
	v_pk_mul_f32 v[60:61], v[0:1], v[60:61]
	v_pk_mul_f32 v[62:63], v[2:3], v[62:63]
	v_cvt_pk_bf16_f32 v60, v60, v61
	v_cvt_pk_bf16_f32 v61, v62, v63
	global_store_dwordx2 v[56:57], v[60:61], off offset:512 nt
	v_pk_mul_f32 v[60:61], v[46:47], v[58:59] op_sel_hi:[1,0]
	v_pk_mul_f32 v[62:63], v[42:43], v[58:59] op_sel_hi:[1,0]
	v_pk_mul_f32 v[60:61], v[4:5], v[60:61]
	v_pk_mul_f32 v[62:63], v[6:7], v[62:63]
	v_cvt_pk_bf16_f32 v60, v60, v61
	v_cvt_pk_bf16_f32 v61, v62, v63
	global_store_dwordx2 v[56:57], v[60:61], off offset:1024 nt
	v_pk_mul_f32 v[60:61], v[44:45], v[58:59] op_sel_hi:[1,0]
	v_pk_mul_f32 v[62:63], v[40:41], v[58:59] op_sel_hi:[1,0]
	v_mul_f32_e32 v58, 0x41800000, v58
	v_mul_f32_e32 v54, v54, v58
	v_mul_f32_e32 v55, v55, v58
	v_mul_f32_e32 v54, v8, v54
	v_mul_f32_e32 v55, v9, v55
	v_mov_b32_e32 v59, v161
	v_mul_f32_e32 v50, v50, v58
	v_mul_f32_e32 v51, v51, v58
	v_cvt_pk_fp8_f32 v59, v54, v55
	v_mul_f32_e32 v50, v0, v50
	v_mul_f32_e32 v51, v1, v51
	v_mov_b32_e32 v54, v161
	v_cvt_pk_fp8_f32 v54, v50, v51
	v_mul_f32_e32 v48, v48, v58
	v_mul_f32_e32 v49, v49, v58
	v_mul_f32_e32 v48, v2, v48
	v_mul_f32_e32 v49, v3, v49
	v_mul_f32_e32 v46, v46, v58
	v_mul_f32_e32 v47, v47, v58
	v_cvt_pk_fp8_f32 v54, v48, v49 op_sel:[0,0,1]
	v_mul_f32_e32 v46, v4, v46
	v_mul_f32_e32 v47, v5, v47
	v_mov_b32_e32 v48, v161
	v_cvt_pk_fp8_f32 v48, v46, v47
	v_mul_f32_e32 v42, v42, v58
	v_mul_f32_e32 v43, v43, v58
	v_mul_f32_e32 v42, v6, v42
	v_mul_f32_e32 v43, v7, v43
	v_cvt_pk_fp8_f32 v48, v42, v43 op_sel:[0,0,1]
	v_mul_f32_e32 v42, v44, v58
	v_mul_f32_e32 v43, v45, v58
	v_mul_f32_e32 v52, v52, v58
	v_mul_f32_e32 v53, v53, v58
	s_waitcnt vmcnt(3)
	v_mul_f32_e32 v42, v12, v42
	v_mul_f32_e32 v43, v13, v43
	v_mov_b32_e32 v44, v161
	v_pk_mul_f32 v[60:61], v[12:13], v[60:61]
	v_pk_mul_f32 v[62:63], v[14:15], v[62:63]
	v_mul_f32_e32 v52, v10, v52
	v_mul_f32_e32 v53, v11, v53
	v_cvt_pk_fp8_f32 v44, v42, v43
	v_cvt_pk_bf16_f32 v60, v60, v61
	v_cvt_pk_bf16_f32 v61, v62, v63
	v_cvt_pk_fp8_f32 v59, v52, v53 op_sel:[0,0,1]
	global_store_dwordx2 v[56:57], v[60:61], off offset:1536 nt
	v_lshl_add_u64 v[56:57], s[36:37], 0, v[38:39]
	v_mul_f32_e32 v40, v40, v58
	v_mul_f32_e32 v41, v41, v58
	v_add_co_u32_e32 v52, vcc, s11, v56
	v_mul_f32_e32 v40, v14, v40
	v_mul_f32_e32 v41, v15, v41
	v_addc_co_u32_e32 v53, vcc, 0, v57, vcc
	v_cvt_pk_fp8_f32 v44, v40, v41 op_sel:[0,0,1]
	global_store_dword v[52:53], v59, off nt
	global_store_dword v[52:53], v54, off offset:256 nt
	global_store_dword v[52:53], v48, off offset:512 nt
	global_store_dword v[52:53], v44, off offset:768 nt
	v_lshl_add_u64 v[38:39], v[38:39], 0, s[4:5]
	s_andn2_b64 vcc, exec, s[2:3]
	v_mov_b32_e32 v54, v18
	v_mov_b32_e32 v55, v21
	v_mov_b32_e32 v52, v24
	v_mov_b32_e32 v53, v25
	v_mov_b32_e32 v50, v16
	v_mov_b32_e32 v51, v17
	v_mov_b32_e32 v48, v20
	v_mov_b32_e32 v49, v19
	v_mov_b32_e32 v46, v22
	v_mov_b32_e32 v47, v23
	v_mov_b32_e32 v42, v26
	v_mov_b32_e32 v43, v27
	v_mov_b32_e32 v44, v28
	v_mov_b32_e32 v45, v29
	v_mov_b32_e32 v40, v30
	v_mov_b32_e32 v41, v31
	s_cbranch_vccz .LBB0_56

.LBB0_60:
	v_mul_f32_e32 v58, v57, v57
	v_mul_f32_e32 v59, v55, v55
	v_fmac_f32_e32 v58, v56, v56
	v_fmac_f32_e32 v59, v54, v54
	v_add_f32_e32 v58, v58, v59
	v_mul_f32_e32 v59, v53, v53
	v_mul_f32_e32 v60, v51, v51
	v_fmac_f32_e32 v59, v52, v52
	v_fmac_f32_e32 v60, v50, v50
	v_add_f32_e32 v59, v59, v60
	v_add_f32_e32 v58, v58, v59
	v_mul_f32_e32 v59, v49, v49
	v_mul_f32_e32 v60, v47, v47
	v_fmac_f32_e32 v59, v48, v48
	v_fmac_f32_e32 v60, v46, v46
	v_add_f32_e32 v59, v59, v60
	v_add_f32_e32 v58, v59, v58
	v_mul_f32_e32 v59, v45, v45
	v_mul_f32_e32 v60, v43, v43
	v_fmac_f32_e32 v59, v44, v44
	v_fmac_f32_e32 v60, v42, v42
	v_add_f32_e32 v59, v59, v60
	v_add_f32_e32 v58, v59, v58
	v_lshl_add_u64 v[60:61], s[36:37], 0, v[38:39]
	v_add_co_u32_e32 v60, vcc, s7, v60
	v_add_f32_dpp v58, v58, v58 quad_perm:[1,0,3,2] row_mask:0xf bank_mask:0xf bound_ctrl:1
	s_nop 0
	v_addc_co_u32_e32 v61, vcc, 0, v61, vcc
	v_add_f32_dpp v58, v58, v58 quad_perm:[2,3,0,1] row_mask:0xf bank_mask:0xf bound_ctrl:1
	s_mov_b64 s[18:19], 0x800000
	s_addk_i32 s6, 0x800
	v_add_f32_dpp v58, v58, v58 row_half_mirror row_mask:0xf bank_mask:0xf bound_ctrl:1
	v_lshl_add_u64 v[38:39], v[38:39], 0, s[22:23]
	v_lshl_add_u64 v[40:41], v[40:41], 0, s[18:19]
	v_add_f32_dpp v58, v58, v58 row_mirror row_mask:0xf bank_mask:0xf bound_ctrl:1
	v_mov_b32_e32 v59, v58
	s_nop 1
	v_permlane16_swap_b32_e32 v58, v59
	v_add_f32_e32 v58, v58, v59
	v_mov_b32_e32 v59, v58
	s_nop 1
	v_permlane32_swap_b32_e32 v58, v59
	v_add_f32_e32 v58, v58, v59
	v_fmamk_f32 v58, v58, 0x3a800000, v240
	v_rsq_f32_e32 v58, v58
	s_nop 0
	v_pk_mul_f32 v[62:63], v[56:57], v[58:59] op_sel_hi:[1,0]
	v_pk_mul_f32 v[64:65], v[54:55], v[58:59] op_sel_hi:[1,0]
	s_waitcnt vmcnt(3)
	v_pk_mul_f32 v[62:63], v[8:9], v[62:63]
	v_pk_mul_f32 v[64:65], v[10:11], v[64:65]
	v_cvt_pk_bf16_f32 v62, v62, v63
	v_cvt_pk_bf16_f32 v63, v64, v65
	global_store_dwordx2 v[60:61], v[62:63], off nt
	v_pk_mul_f32 v[62:63], v[52:53], v[58:59] op_sel_hi:[1,0]
	v_pk_mul_f32 v[64:65], v[50:51], v[58:59] op_sel_hi:[1,0]
	s_waitcnt vmcnt(3)
	v_pk_mul_f32 v[62:63], v[16:17], v[62:63]
	v_pk_mul_f32 v[64:65], v[18:19], v[64:65]
	v_cvt_pk_bf16_f32 v62, v62, v63
	v_cvt_pk_bf16_f32 v63, v64, v65
	global_store_dwordx2 v[60:61], v[62:63], off offset:512 nt
	v_pk_mul_f32 v[62:63], v[48:49], v[58:59] op_sel_hi:[1,0]
	v_pk_mul_f32 v[64:65], v[46:47], v[58:59] op_sel_hi:[1,0]
	s_waitcnt vmcnt(3)
	v_pk_mul_f32 v[62:63], v[20:21], v[62:63]
	v_pk_mul_f32 v[64:65], v[22:23], v[64:65]
	v_cvt_pk_bf16_f32 v62, v62, v63
	v_cvt_pk_bf16_f32 v63, v64, v65
	global_store_dwordx2 v[60:61], v[62:63], off offset:1024 nt
	v_pk_mul_f32 v[62:63], v[44:45], v[58:59] op_sel_hi:[1,0]
	v_pk_mul_f32 v[64:65], v[42:43], v[58:59] op_sel_hi:[1,0]
	v_mul_f32_e32 v58, 0x41800000, v58
	v_mul_f32_e32 v56, v56, v58
	v_mul_f32_e32 v57, v57, v58
	v_mul_f32_e32 v56, v8, v56
	v_mul_f32_e32 v57, v9, v57
	v_mov_b32_e32 v59, v161
	v_mul_f32_e32 v52, v52, v58
	v_mul_f32_e32 v53, v53, v58
	v_cvt_pk_fp8_f32 v59, v56, v57
	v_mul_f32_e32 v52, v16, v52
	v_mul_f32_e32 v53, v17, v53
	v_mov_b32_e32 v56, v161
	v_cvt_pk_fp8_f32 v56, v52, v53
	v_mul_f32_e32 v50, v50, v58
	v_mul_f32_e32 v51, v51, v58
	v_mul_f32_e32 v50, v18, v50
	v_mul_f32_e32 v51, v19, v51
	v_mul_f32_e32 v48, v48, v58
	v_mul_f32_e32 v49, v49, v58
	v_cvt_pk_fp8_f32 v56, v50, v51 op_sel:[0,0,1]
	v_mul_f32_e32 v48, v20, v48
	v_mul_f32_e32 v49, v21, v49
	v_mov_b32_e32 v50, v161
	v_cvt_pk_fp8_f32 v50, v48, v49
	v_mul_f32_e32 v46, v46, v58
	v_mul_f32_e32 v47, v47, v58
	v_mul_f32_e32 v46, v22, v46
	v_mul_f32_e32 v47, v23, v47
	v_mul_f32_e32 v44, v44, v58
	v_mul_f32_e32 v45, v45, v58
	v_mul_f32_e32 v54, v54, v58
	v_mul_f32_e32 v55, v55, v58
	v_cvt_pk_fp8_f32 v50, v46, v47 op_sel:[0,0,1]
	s_waitcnt vmcnt(3)
	v_mul_f32_e32 v44, v24, v44
	v_mul_f32_e32 v45, v25, v45
	v_mov_b32_e32 v46, v161
	v_pk_mul_f32 v[62:63], v[24:25], v[62:63]
	v_pk_mul_f32 v[64:65], v[26:27], v[64:65]
	v_mul_f32_e32 v54, v10, v54
	v_mul_f32_e32 v55, v11, v55
	v_cvt_pk_fp8_f32 v46, v44, v45
	v_cvt_pk_bf16_f32 v62, v62, v63
	v_cvt_pk_bf16_f32 v63, v64, v65
	v_cvt_pk_fp8_f32 v59, v54, v55 op_sel:[0,0,1]
	global_store_dwordx2 v[60:61], v[62:63], off offset:1536 nt
	v_lshl_add_u64 v[60:61], s[36:37], 0, v[36:37]
	v_mul_f32_e32 v42, v42, v58
	v_mul_f32_e32 v43, v43, v58
	v_add_co_u32_e32 v54, vcc, s10, v60
	v_mul_f32_e32 v42, v26, v42
	v_mul_f32_e32 v43, v27, v43
	v_addc_co_u32_e32 v55, vcc, 0, v61, vcc
	v_cvt_pk_fp8_f32 v46, v42, v43 op_sel:[0,0,1]
	global_store_dword v[54:55], v59, off nt
	global_store_dword v[54:55], v56, off offset:256 nt
	global_store_dword v[54:55], v50, off offset:512 nt
	global_store_dword v[54:55], v46, off offset:768 nt
	v_lshl_add_u64 v[36:37], v[36:37], 0, s[4:5]
	s_and_b64 vcc, exec, s[2:3]
	v_mov_b32_e32 v56, v0
	v_mov_b32_e32 v57, v1
	v_mov_b32_e32 v54, v2
	v_mov_b32_e32 v55, v3
	v_mov_b32_e32 v52, v4
	v_mov_b32_e32 v53, v5
	v_mov_b32_e32 v50, v6
	v_mov_b32_e32 v51, v7
	v_mov_b32_e32 v48, v12
	v_mov_b32_e32 v49, v13
	v_mov_b32_e32 v46, v14
	v_mov_b32_e32 v47, v15
	v_mov_b32_e32 v44, v28
	v_mov_b32_e32 v45, v29
	v_mov_b32_e32 v42, v30
	v_mov_b32_e32 v43, v31
	s_cbranch_vccnz .LBB0_63

.LBB0_65:
	v_mul_f32_e32 v35, v55, v55
	v_mul_f32_e32 v56, v53, v53
	v_fmac_f32_e32 v35, v54, v54
	v_fmac_f32_e32 v56, v52, v52
	v_add_f32_e32 v35, v35, v56
	v_mul_f32_e32 v56, v51, v51
	v_mul_f32_e32 v57, v49, v49
	v_fmac_f32_e32 v56, v50, v50
	v_fmac_f32_e32 v57, v48, v48
	v_add_f32_e32 v56, v56, v57
	v_add_f32_e32 v35, v35, v56
	v_mul_f32_e32 v56, v47, v47
	v_mul_f32_e32 v57, v45, v45
	v_fmac_f32_e32 v56, v46, v46
	v_fmac_f32_e32 v57, v44, v44
	v_add_f32_e32 v56, v56, v57
	v_add_f32_e32 v35, v56, v35
	v_mul_f32_e32 v56, v43, v43
	v_mul_f32_e32 v57, v41, v41
	v_fmac_f32_e32 v56, v42, v42
	v_fmac_f32_e32 v57, v40, v40
	v_add_f32_e32 v56, v56, v57
	v_add_f32_e32 v35, v56, v35
	s_mov_b64 s[4:5], 0x800000
	s_addk_i32 s6, 0x800
	v_add_f32_dpp v35, v35, v35 quad_perm:[1,0,3,2] row_mask:0xf bank_mask:0xf bound_ctrl:1
	v_lshl_add_u64 v[36:37], v[36:37], 0, s[4:5]
	s_andn2_b64 vcc, exec, s[2:3]
	v_add_f32_dpp v35, v35, v35 quad_perm:[2,3,0,1] row_mask:0xf bank_mask:0xf bound_ctrl:1
	s_nop 1
	v_add_f32_dpp v35, v35, v35 row_half_mirror row_mask:0xf bank_mask:0xf bound_ctrl:1
	s_nop 1
	v_add_f32_dpp v35, v35, v35 row_mirror row_mask:0xf bank_mask:0xf bound_ctrl:1
	v_mov_b32_e32 v56, v35
	s_nop 1
	v_permlane16_swap_b32_e32 v35, v56
	v_add_f32_e32 v35, v35, v56
	v_mov_b32_e32 v56, v35
	s_nop 1
	v_permlane32_swap_b32_e32 v35, v56
	v_add_f32_e32 v35, v35, v56
	v_fmamk_f32 v35, v35, 0x3a800000, v240
	v_rsq_f32_e32 v56, v35
	s_nop 0
	v_pk_mul_f32 v[54:55], v[54:55], v[56:57] op_sel_hi:[1,0]
	v_pk_mul_f32 v[52:53], v[52:53], v[56:57] op_sel_hi:[1,0]
	v_pk_mul_f32 v[50:51], v[50:51], v[56:57] op_sel_hi:[1,0]
	v_pk_mul_f32 v[48:49], v[48:49], v[56:57] op_sel_hi:[1,0]
	v_pk_mul_f32 v[46:47], v[46:47], v[56:57] op_sel_hi:[1,0]
	v_pk_mul_f32 v[44:45], v[44:45], v[56:57] op_sel_hi:[1,0]
	v_pk_mul_f32 v[42:43], v[42:43], v[56:57] op_sel_hi:[1,0]
	v_pk_mul_f32 v[40:41], v[40:41], v[56:57] op_sel_hi:[1,0]
	s_waitcnt vmcnt(0)
	v_pk_mul_f32 v[54:55], v[24:25], v[54:55]
	v_pk_mul_f32 v[52:53], v[26:27], v[52:53]
	v_pk_mul_f32 v[50:51], v[20:21], v[50:51]
	v_pk_mul_f32 v[48:49], v[22:23], v[48:49]
	v_pk_mul_f32 v[46:47], v[16:17], v[46:47]
	v_pk_mul_f32 v[44:45], v[18:19], v[44:45]
	v_pk_mul_f32 v[42:43], v[8:9], v[42:43]
	v_pk_mul_f32 v[40:41], v[10:11], v[40:41]
	v_cvt_pk_bf16_f32 v54, v54, v55
	v_cvt_pk_bf16_f32 v55, v52, v53
	v_cvt_pk_bf16_f32 v50, v50, v51
	v_cvt_pk_bf16_f32 v51, v48, v49
	v_cvt_pk_bf16_f32 v46, v46, v47
	v_cvt_pk_bf16_f32 v47, v44, v45
	v_cvt_pk_bf16_f32 v42, v42, v43
	v_cvt_pk_bf16_f32 v43, v40, v41
	global_store_dwordx2 v[38:39], v[54:55], off nt
	global_store_dwordx2 v[38:39], v[50:51], off offset:512 nt
	global_store_dwordx2 v[38:39], v[46:47], off offset:1024 nt
	global_store_dwordx2 v[38:39], v[42:43], off offset:1536 nt
	v_lshl_add_u64 v[38:39], v[38:39], 0, s[22:23]
	v_mov_b32_e32 v54, v0
	v_mov_b32_e32 v55, v1
	v_mov_b32_e32 v52, v2
	v_mov_b32_e32 v53, v3
	v_mov_b32_e32 v50, v4
	v_mov_b32_e32 v51, v5
	v_mov_b32_e32 v48, v6
	v_mov_b32_e32 v49, v7
	v_mov_b32_e32 v46, v12
	v_mov_b32_e32 v47, v13
	v_mov_b32_e32 v44, v14
	v_mov_b32_e32 v45, v15
	v_mov_b32_e32 v42, v28
	v_mov_b32_e32 v43, v29
	v_mov_b32_e32 v40, v30
	v_mov_b32_e32 v41, v31
	s_cbranch_vccz .LBB0_68

.LBB0_269:
	v_lshlrev_b32_e32 v78, 16, v63
	v_and_b32_e32 v79, 0xffff0000, v63
	v_lshlrev_b32_e32 v84, 16, v62
	v_and_b32_e32 v85, 0xffff0000, v62
	v_lshlrev_b32_e32 v62, 16, v60
	v_and_b32_e32 v63, 0xffff0000, v60
	v_lshlrev_b32_e32 v80, 16, v61
	v_and_b32_e32 v81, 0xffff0000, v61
	v_pk_mul_f32 v[60:61], v[62:63], v[62:63]
	v_pk_mul_f32 v[82:83], v[80:81], v[80:81]
	v_pk_fma_f32 v[60:61], v[84:85], v[84:85], v[60:61]
	v_pk_fma_f32 v[82:83], v[78:79], v[78:79], v[82:83]
	v_add_f32_e32 v60, v60, v61
	v_add_f32_e32 v60, v60, v82
	v_add_f32_e32 v60, v60, v83
	s_mov_b32 s22, 0x6400000
	s_addk_i32 s11, 0x800
	v_add_f32_dpp v60, v60, v60 quad_perm:[1,0,3,2] row_mask:0xf bank_mask:0xf bound_ctrl:1
	s_add_i32 s10, s10, 0x10000
	s_add_i32 s7, s7, 0x8000
	v_add_f32_dpp v60, v60, v60 quad_perm:[2,3,0,1] row_mask:0xf bank_mask:0xf bound_ctrl:1
	s_nop 1
	v_add_f32_dpp v60, v60, v60 row_half_mirror row_mask:0xf bank_mask:0xf bound_ctrl:1
	v_fmamk_f32 v60, v60, 0x3c800000, v240
	v_rsq_f32_e32 v60, v60
	s_nop 0
	v_pk_mul_f32 v[62:63], v[60:61], v[62:63] op_sel_hi:[0,1]
	v_pk_mul_f32 v[82:83], v[60:61], v[84:85] op_sel_hi:[0,1]
	v_pk_mul_f32 v[62:63], v[4:5], v[62:63]
	v_pk_mul_f32 v[82:83], v[0:1], v[82:83]
	v_pk_mul_f32 v[84:85], v[8:9], v[62:63]
	s_nop 0
	v_pk_fma_f32 v[84:85], v[12:13], v[82:83], v[84:85] neg_lo:[0,0,1] neg_hi:[0,0,1]
	v_pk_mul_f32 v[12:13], v[12:13], v[62:63]
	s_nop 0
	v_pk_fma_f32 v[8:9], v[8:9], v[82:83], v[12:13]
	v_pk_mul_f32 v[12:13], v[60:61], v[78:79] op_sel_hi:[0,1]
	v_pk_mul_f32 v[60:61], v[60:61], v[80:81] op_sel_hi:[0,1]
	v_pk_mul_f32 v[60:61], v[6:7], v[60:61]
	v_pk_mul_f32 v[12:13], v[2:3], v[12:13]
	v_pk_mul_f32 v[62:63], v[10:11], v[60:61]
	v_cvt_pk_bf16_f32 v8, v8, v9
	v_pk_fma_f32 v[62:63], v[14:15], v[12:13], v[62:63] neg_lo:[0,0,1] neg_hi:[0,0,1]
	v_pk_mul_f32 v[14:15], v[14:15], v[60:61]
	s_nop 0
	v_pk_fma_f32 v[10:11], v[10:11], v[12:13], v[14:15]
	v_lshlrev_b32_e32 v14, 16, v76
	v_and_b32_e32 v15, 0xffff0000, v76
	v_pk_mul_f32 v[60:61], v[14:15], v[14:15]
	v_cvt_pk_bf16_f32 v9, v10, v11
	v_add_f32_e32 v13, v60, v61
	v_cvt_pk_bf16_f32 v12, v84, v85
	s_nop 0
	v_add_f32_dpp v13, v13, v13 quad_perm:[1,0,3,2] row_mask:0xf bank_mask:0xf bound_ctrl:1
	s_nop 1
	v_add_f32_dpp v13, v13, v13 quad_perm:[2,3,0,1] row_mask:0xf bank_mask:0xf bound_ctrl:1
	s_nop 1
	v_add_f32_dpp v13, v13, v13 row_half_mirror row_mask:0xf bank_mask:0xf bound_ctrl:1
	s_nop 1
	v_add_f32_dpp v13, v13, v13 row_mirror row_mask:0xf bank_mask:0xf bound_ctrl:1
	v_mov_b32_e32 v60, v13
	s_nop 1
	v_permlane16_swap_b32_e32 v13, v60
	v_add_f32_e32 v13, v13, v60
	v_fmamk_f32 v13, v13, 0x3c800000, v240
	v_rsq_f32_e32 v60, v13
	v_cvt_pk_bf16_f32 v13, v62, v63
	v_pk_mul_f32 v[10:11], v[60:61], v[14:15] op_sel_hi:[0,1]
	v_pk_mul_f32 v[10:11], v[28:29], v[10:11]
	v_lshlrev_b32_e32 v60, 16, v70
	v_and_b32_e32 v61, 0xffff0000, v70
	v_mov_b32_dpp v14, v10 row_ror:8 row_mask:0xf bank_mask:0xf bound_ctrl:1
	v_mov_b32_dpp v15, v11 row_ror:8 row_mask:0xf bank_mask:0xf bound_ctrl:1
	v_pk_mul_f32 v[14:15], v[50:51], v[14:15]
	v_lshlrev_b32_e32 v50, 16, v73
	v_and_b32_e32 v51, 0xffff0000, v73
	v_pk_mul_f32 v[76:77], v[50:51], v[50:51]
	v_pk_mul_f32 v[62:63], v[60:61], v[60:61]
	v_add_f32_e32 v70, v76, v77
	v_add_f32_e32 v62, v70, v62
	v_add_f32_e32 v62, v63, v62
	v_cndmask_b32_e64 v15, v15, -v15, s[42:43]
	v_cndmask_b32_e64 v14, v14, -v14, s[42:43]
	v_add_f32_dpp v62, v62, v62 quad_perm:[1,0,3,2] row_mask:0xf bank_mask:0xf bound_ctrl:1
	v_pk_fma_f32 v[10:11], v[44:45], v[10:11], v[14:15]
	s_waitcnt vmcnt(7)
	v_mov_b32_e32 v73, v71
	v_add_f32_dpp v62, v62, v62 quad_perm:[2,3,0,1] row_mask:0xf bank_mask:0xf bound_ctrl:1
	s_waitcnt vmcnt(6)
	v_mov_b32_e32 v70, v72
	s_waitcnt vmcnt(4)
	v_mov_b32_e32 v76, v75
	v_add_f32_dpp v62, v62, v62 row_half_mirror row_mask:0xf bank_mask:0xf bound_ctrl:1
	s_nop 1
	v_add_f32_dpp v62, v62, v62 row_mirror row_mask:0xf bank_mask:0xf bound_ctrl:1
	v_mov_b32_e32 v63, v62
	s_nop 1
	v_permlane16_swap_b32_e32 v62, v63
	v_add_f32_e32 v62, v62, v63
	v_mov_b32_e32 v63, v62
	s_nop 1
	v_permlane32_swap_b32_e32 v62, v63
	v_add_f32_e32 v62, v62, v63
	v_fmamk_f32 v62, v62, 0x3b800000, v240
	v_rsq_f32_e32 v62, v62
	v_cvt_pk_bf16_f32 v63, v10, v11
	v_pk_mul_f32 v[10:11], v[62:63], v[50:51] op_sel_hi:[0,1]
	v_pk_mul_f32 v[10:11], v[30:31], v[10:11]
	v_pk_mul_f32 v[44:45], v[62:63], v[60:61] op_sel_hi:[0,1]
	v_cvt_pk_bf16_f32 v50, v10, v11
	v_lshlrev_b32_e32 v10, 16, v69
	v_and_b32_e32 v11, 0xffff0000, v69
	v_pk_mul_f32 v[14:15], v[10:11], v[10:11]
	v_pk_mul_f32 v[44:45], v[32:33], v[44:45]
	v_add_f32_e32 v14, v14, v15
	v_mov_b32_e32 v69, v74
	v_mov_b64_e32 v[60:61], v[56:57]
	v_add_f32_dpp v14, v14, v14 quad_perm:[1,0,3,2] row_mask:0xf bank_mask:0xf bound_ctrl:1
	s_nop 1
	v_add_f32_dpp v14, v14, v14 quad_perm:[2,3,0,1] row_mask:0xf bank_mask:0xf bound_ctrl:1
	s_nop 1
	v_add_f32_dpp v14, v14, v14 row_half_mirror row_mask:0xf bank_mask:0xf bound_ctrl:1
	s_nop 1
	v_add_f32_dpp v14, v14, v14 row_mirror row_mask:0xf bank_mask:0xf bound_ctrl:1
	v_mov_b32_e32 v15, v14
	s_nop 1
	v_permlane16_swap_b32_e32 v14, v15
	v_add_f32_e32 v14, v14, v15
	v_mov_b32_e32 v15, v14
	s_nop 1
	v_permlane32_swap_b32_e32 v14, v15
	v_add_f32_e32 v14, v14, v15
	v_fmamk_f32 v14, v14, 0x3c000000, v240
	v_rsq_f32_e32 v14, v14
	v_cvt_pk_bf16_f32 v15, v44, v45
	s_waitcnt vmcnt(1)
	v_mov_b64_e32 v[44:45], v[52:53]
	v_pk_mul_f32 v[10:11], v[14:15], v[10:11] op_sel_hi:[0,1]
	s_waitcnt vmcnt(0)
	v_pk_mul_f32 v[10:11], v[40:41], v[10:11]
	s_nop 0
	v_cvt_pk_bf16_f32 v14, v10, v11
	v_add_co_u32_e32 v10, vcc, s22, v66
	s_mov_b32 s22, 0x6401000
	s_nop 0
	v_addc_co_u32_e32 v11, vcc, 0, v67, vcc
	global_store_dwordx2 v[10:11], v[12:13], off offset:1024 nt
	global_store_dwordx2 v[10:11], v[8:9], off offset:1088 nt
	v_add_co_u32_e32 v8, vcc, s22, v64
	s_mov_b64 s[22:23], 0xd00000
	s_nop 0
	v_addc_co_u32_e32 v9, vcc, 0, v65, vcc
	global_store_dword v[8:9], v63, off offset:1024 nt
	v_lshl_add_u64 v[8:9], s[18:19], 0, v[42:43]
	v_add_co_u32_e32 v8, vcc, 0x1d400000, v8
	v_lshl_add_u64 v[42:43], v[42:43], 0, s[4:5]
	s_nop 0
	v_addc_co_u32_e32 v9, vcc, 0, v9, vcc
	global_store_dword v[8:9], v50, off nt
	global_store_dword v[8:9], v15, off offset:256 nt
	global_store_dword v[8:9], v14, off offset:512 nt
	global_store_dword v[8:9], v161, off offset:768 nt
	v_mov_b64_e32 v[12:13], v[16:17]
	v_mov_b64_e32 v[8:9], v[20:21]
	v_lshl_add_u64 v[46:47], v[46:47], 0, s[22:23]
	v_lshl_add_u64 v[48:49], v[48:49], 0, s[22:23]
	s_and_b64 vcc, exec, s[2:3]
	v_mov_b64_e32 v[62:63], v[58:59]
	v_mov_b64_e32 v[14:15], v[18:19]
	v_mov_b64_e32 v[10:11], v[22:23]
	v_mov_b64_e32 v[50:51], v[54:55]
	s_cbranch_vccnz .LBB0_272

.LBB0_274:
	global_load_dword v10, v[4:5], off
	global_load_dword v16, v[4:5], off offset:512
	global_load_dword v17, v[4:5], off offset:1024
	global_load_dword v11, v[4:5], off offset:1536
	s_and_b32 s6, s3, 0x3fc0
	s_lshl_b32 s96, s6, 2
	v_lshl_add_u64 v[6:7], v[0:1], 0, s[96:97]
	v_lshl_add_u64 v[8:9], v[2:3], 0, s[96:97]
	global_load_dwordx2 v[6:7], v[6:7], off
	s_addk_i32 s2, 0x800
	global_load_dwordx2 v[8:9], v[8:9], off
	s_add_i32 s3, s3, 0x20000
	s_cmpk_gt_i32 s2, 0x7ff
	s_waitcnt vmcnt(5)
	v_lshlrev_b32_e32 v12, 16, v10
	v_and_b32_e32 v13, 0xffff0000, v10
	v_pk_mul_f32 v[14:15], v[12:13], v[12:13]
	s_nop 0
	v_add_f32_e32 v10, v14, v15
	s_nop 1
	v_add_f32_dpp v10, v10, v10 quad_perm:[1,0,3,2] row_mask:0xf bank_mask:0xf bound_ctrl:1
	s_nop 1
	v_add_f32_dpp v10, v10, v10 quad_perm:[2,3,0,1] row_mask:0xf bank_mask:0xf bound_ctrl:1
	s_nop 1
	v_add_f32_dpp v10, v10, v10 row_half_mirror row_mask:0xf bank_mask:0xf bound_ctrl:1
	s_nop 1
	v_add_f32_dpp v10, v10, v10 row_mirror row_mask:0xf bank_mask:0xf bound_ctrl:1
	v_mov_b32_e32 v14, v10
	s_nop 1
	v_permlane16_swap_b32_e32 v10, v14
	v_add_f32_e32 v10, v10, v14
	v_mov_b32_e32 v14, v10
	s_nop 1
	v_permlane32_swap_b32_e32 v10, v14
	v_add_f32_e32 v10, v10, v14
	v_fmamk_f32 v10, v10, 0x3c000000, v240
	v_rsq_f32_e32 v10, v10
	s_waitcnt vmcnt(2)
	v_pk_mul_f32 v[12:13], v[10:11], v[12:13] op_sel_hi:[0,1]
	v_pk_mul_f32 v[12:13], v[24:25], v[12:13]
	s_nop 0
	v_mov_b32_e32 v10, v12
	v_mov_b32_e32 v14, v12
	v_mov_b32_e32 v15, v13
	v_mov_b32_e32 v18, v13
	v_permlane32_swap_b32_e32 v10, v14
	s_nop 0
	v_permlane32_swap_b32_e32 v15, v18
	v_cndmask_b32_e32 v15, v15, v18, vcc
	v_cndmask_b32_e32 v14, v10, v14, vcc
	s_waitcnt vmcnt(0)
	v_pk_mul_f32 v[14:15], v[8:9], v[14:15]
	s_nop 0
	v_cndmask_b32_e64 v15, v15, -v15, s[40:41]
	v_cndmask_b32_e64 v14, v14, -v14, s[40:41]
	v_pk_fma_f32 v[12:13], v[6:7], v[12:13], v[14:15]
	s_nop 0
	v_cvt_pk_bf16_f32 v10, v12, v13
	v_lshlrev_b32_e32 v12, 16, v16
	v_and_b32_e32 v13, 0xffff0000, v16
	v_pk_mul_f32 v[14:15], v[12:13], v[12:13]
	s_nop 0
	v_add_f32_e32 v14, v14, v15
	s_nop 1
	v_add_f32_dpp v14, v14, v14 quad_perm:[1,0,3,2] row_mask:0xf bank_mask:0xf bound_ctrl:1
	s_nop 1
	v_add_f32_dpp v14, v14, v14 quad_perm:[2,3,0,1] row_mask:0xf bank_mask:0xf bound_ctrl:1
	s_nop 1
	v_add_f32_dpp v14, v14, v14 row_half_mirror row_mask:0xf bank_mask:0xf bound_ctrl:1
	s_nop 1
	v_add_f32_dpp v14, v14, v14 row_mirror row_mask:0xf bank_mask:0xf bound_ctrl:1
	v_mov_b32_e32 v15, v14
	s_nop 1
	v_permlane16_swap_b32_e32 v14, v15
	v_add_f32_e32 v14, v14, v15
	v_mov_b32_e32 v15, v14
	s_nop 1
	v_permlane32_swap_b32_e32 v14, v15
	v_add_f32_e32 v14, v14, v15
	v_fmamk_f32 v14, v14, 0x3c000000, v240
	v_rsq_f32_e32 v14, v14
	s_nop 0
	v_pk_mul_f32 v[12:13], v[14:15], v[12:13] op_sel_hi:[0,1]
	v_pk_mul_f32 v[12:13], v[24:25], v[12:13]
	s_nop 0
	v_mov_b32_e32 v14, v12
	v_mov_b32_e32 v16, v12
	v_mov_b32_e32 v15, v13
	v_mov_b32_e32 v18, v13
	v_permlane32_swap_b32_e32 v14, v16
	s_nop 0
	v_permlane32_swap_b32_e32 v15, v18
	v_cndmask_b32_e32 v15, v15, v18, vcc
	v_cndmask_b32_e32 v14, v14, v16, vcc
	v_pk_mul_f32 v[14:15], v[8:9], v[14:15]
	s_nop 0
	v_cndmask_b32_e64 v15, v15, -v15, s[40:41]
	v_cndmask_b32_e64 v14, v14, -v14, s[40:41]
	v_pk_fma_f32 v[12:13], v[6:7], v[12:13], v[14:15]
	s_nop 0
	v_cvt_pk_bf16_f32 v16, v12, v13
	v_lshlrev_b32_e32 v12, 16, v17
	v_and_b32_e32 v13, 0xffff0000, v17
	v_pk_mul_f32 v[14:15], v[12:13], v[12:13]
	s_nop 0
	v_add_f32_e32 v14, v14, v15
	s_nop 1
	v_add_f32_dpp v14, v14, v14 quad_perm:[1,0,3,2] row_mask:0xf bank_mask:0xf bound_ctrl:1
	s_nop 1
	v_add_f32_dpp v14, v14, v14 quad_perm:[2,3,0,1] row_mask:0xf bank_mask:0xf bound_ctrl:1
	s_nop 1
	v_add_f32_dpp v14, v14, v14 row_half_mirror row_mask:0xf bank_mask:0xf bound_ctrl:1
	s_nop 1
	v_add_f32_dpp v14, v14, v14 row_mirror row_mask:0xf bank_mask:0xf bound_ctrl:1
	v_mov_b32_e32 v15, v14
	s_nop 1
	v_permlane16_swap_b32_e32 v14, v15
	v_add_f32_e32 v14, v14, v15
	v_mov_b32_e32 v15, v14
	s_nop 1
	v_permlane32_swap_b32_e32 v14, v15
	v_add_f32_e32 v14, v14, v15
	v_fmamk_f32 v14, v14, 0x3c000000, v240
	v_rsq_f32_e32 v14, v14
	s_nop 0
	v_pk_mul_f32 v[12:13], v[14:15], v[12:13] op_sel_hi:[0,1]
	v_pk_mul_f32 v[12:13], v[24:25], v[12:13]
	s_nop 0
	v_mov_b32_e32 v14, v12
	v_mov_b32_e32 v17, v12
	v_mov_b32_e32 v15, v13
	v_mov_b32_e32 v18, v13
	v_permlane32_swap_b32_e32 v14, v17
	s_nop 0
	v_permlane32_swap_b32_e32 v15, v18
	v_cndmask_b32_e32 v15, v15, v18, vcc
	v_cndmask_b32_e32 v14, v14, v17, vcc
	v_pk_mul_f32 v[14:15], v[8:9], v[14:15]
	s_nop 0
	v_cndmask_b32_e64 v15, v15, -v15, s[40:41]
	v_cndmask_b32_e64 v14, v14, -v14, s[40:41]
	v_pk_fma_f32 v[12:13], v[6:7], v[12:13], v[14:15]
	s_nop 0
	v_cvt_pk_bf16_f32 v17, v12, v13
	v_lshlrev_b32_e32 v12, 16, v11
	v_and_b32_e32 v13, 0xffff0000, v11
	v_pk_mul_f32 v[14:15], v[12:13], v[12:13]
	s_nop 0
	v_add_f32_e32 v11, v14, v15
	s_nop 1
	v_add_f32_dpp v11, v11, v11 quad_perm:[1,0,3,2] row_mask:0xf bank_mask:0xf bound_ctrl:1
	s_nop 1
	v_add_f32_dpp v11, v11, v11 quad_perm:[2,3,0,1] row_mask:0xf bank_mask:0xf bound_ctrl:1
	s_nop 1
	v_add_f32_dpp v11, v11, v11 row_half_mirror row_mask:0xf bank_mask:0xf bound_ctrl:1
	s_nop 1
	v_add_f32_dpp v11, v11, v11 row_mirror row_mask:0xf bank_mask:0xf bound_ctrl:1
	v_mov_b32_e32 v14, v11
	s_nop 1
	v_permlane16_swap_b32_e32 v11, v14
	v_add_f32_e32 v11, v11, v14
	v_mov_b32_e32 v14, v11
	s_nop 1
	v_permlane32_swap_b32_e32 v11, v14
	v_add_f32_e32 v11, v11, v14
	v_fmamk_f32 v11, v11, 0x3c000000, v240
	v_rsq_f32_e32 v14, v11
	s_nop 0
	v_pk_mul_f32 v[12:13], v[14:15], v[12:13] op_sel_hi:[0,1]
	v_pk_mul_f32 v[12:13], v[24:25], v[12:13]
	s_nop 0
	v_mov_b32_e32 v11, v12
	v_mov_b32_e32 v14, v12
	v_mov_b32_e32 v15, v13
	v_mov_b32_e32 v18, v13
	v_permlane32_swap_b32_e32 v11, v14
	s_nop 0
	v_permlane32_swap_b32_e32 v15, v18
	v_cndmask_b32_e32 v15, v15, v18, vcc
	v_cndmask_b32_e32 v14, v11, v14, vcc
	v_pk_mul_f32 v[8:9], v[8:9], v[14:15]
	s_nop 0
	v_cndmask_b32_e64 v9, v9, -v9, s[40:41]
	v_cndmask_b32_e64 v8, v8, -v8, s[40:41]
	v_pk_fma_f32 v[6:7], v[6:7], v[12:13], v[8:9]
	s_nop 0
	v_cvt_pk_bf16_f32 v6, v6, v7
	global_store_dword v[4:5], v10, off nt
	global_store_dword v[4:5], v16, off offset:512 nt
	global_store_dword v[4:5], v17, off offset:1024 nt
	global_store_dword v[4:5], v6, off offset:1536 nt
	v_lshl_add_u64 v[4:5], v[4:5], 0, s[10:11]
	s_cbranch_scc0 .LBB0_274

.LBB0_402:
	v_lshlrev_b32_e32 v68, 16, v32
	v_and_b32_e32 v69, 0xffff0000, v32
	v_lshlrev_b32_e32 v64, 16, v33
	v_and_b32_e32 v65, 0xffff0000, v33
	v_pk_mul_f32 v[32:33], v[68:69], v[68:69]
	v_pk_mul_f32 v[66:67], v[64:65], v[64:65]
	v_add_f32_e32 v32, v32, v33
	v_lshlrev_b32_e32 v62, 16, v34
	v_and_b32_e32 v63, 0xffff0000, v34
	v_add_f32_e32 v32, v32, v66
	v_lshlrev_b32_e32 v58, 16, v35
	v_and_b32_e32 v59, 0xffff0000, v35
	v_pk_mul_f32 v[34:35], v[62:63], v[62:63]
	v_add_f32_e32 v32, v32, v67
	v_add_f32_e32 v32, v32, v34
	v_pk_mul_f32 v[60:61], v[58:59], v[58:59]
	v_add_f32_e32 v32, v32, v35
	v_lshlrev_b32_e32 v52, 16, v50
	v_and_b32_e32 v53, 0xffff0000, v50
	v_add_f32_e32 v32, v32, v60
	v_pk_mul_f32 v[54:55], v[52:53], v[52:53]
	v_add_f32_e32 v32, v32, v61
	v_lshlrev_b32_e32 v50, 16, v51
	v_and_b32_e32 v51, 0xffff0000, v51
	v_add_f32_e32 v32, v32, v54
	v_pk_mul_f32 v[56:57], v[50:51], v[50:51]
	v_add_f32_e32 v32, v32, v55
	v_add_f32_e32 v32, v32, v56
	v_add_f32_e32 v32, v32, v57
	s_mov_b64 s[4:5], 0x300000
	s_addk_i32 s6, 0x800
	v_add_f32_dpp v32, v32, v32 quad_perm:[1,0,3,2] row_mask:0xf bank_mask:0xf bound_ctrl:1
	s_add_i32 s7, s7, 0x8000
	s_and_b64 vcc, exec, s[22:23]
	v_add_f32_dpp v32, v32, v32 quad_perm:[2,3,0,1] row_mask:0xf bank_mask:0xf bound_ctrl:1
	s_nop 1
	v_add_f32_dpp v32, v32, v32 row_half_mirror row_mask:0xf bank_mask:0xf bound_ctrl:1
	v_fmamk_f32 v32, v32, 0x3c2aaaab, v240
	v_rsq_f32_e32 v54, v32
	s_nop 0
	v_pk_mul_f32 v[32:33], v[54:55], v[68:69] op_sel_hi:[0,1]
	v_pk_mul_f32 v[34:35], v[54:55], v[64:65] op_sel_hi:[0,1]
	s_waitcnt vmcnt(1)
	v_pk_mul_f32 v[32:33], v[12:13], v[32:33]
	v_pk_mul_f32 v[34:35], v[14:15], v[34:35]
	v_mul_f32_e32 v52, v54, v52
	v_cvt_pk_bf16_f32 v32, v32, v33
	v_cvt_pk_bf16_f32 v33, v34, v35
	v_pk_mul_f32 v[34:35], v[54:55], v[62:63] op_sel_hi:[0,1]
	v_pk_mul_f32 v[56:57], v[54:55], v[58:59] op_sel_hi:[0,1]
	v_mul_f32_e32 v55, v0, v52
	v_mul_f32_e32 v52, v54, v53
	v_mul_f32_e32 v52, v1, v52
	v_mov_b32_dpp v53, v55 row_half_mirror row_mask:0xf bank_mask:0xf bound_ctrl:1
	v_pk_mul_f32 v[50:51], v[54:55], v[50:51] op_sel_hi:[0,1]
	v_pk_mul_f32 v[50:51], v[2:3], v[50:51]
	v_mul_f32_dpp v4, v53, v4 quad_perm:[3,2,1,0] row_mask:0xf bank_mask:0xf bound_ctrl:1
	v_cndmask_b32_e64 v54, v4, -v4, s[40:41]
	v_fmac_f32_e32 v54, v8, v55
	v_mov_b32_dpp v4, v52 row_half_mirror row_mask:0xf bank_mask:0xf bound_ctrl:1
	s_waitcnt vmcnt(0)
	v_pk_mul_f32 v[34:35], v[16:17], v[34:35]
	v_pk_mul_f32 v[56:57], v[18:19], v[56:57]
	v_mov_b32_dpp v53, v4 quad_perm:[3,2,1,0] row_mask:0xf bank_mask:0xf bound_ctrl:1
	v_mov_b32_e32 v4, v9
	v_pk_mul_f32 v[4:5], v[4:5], v[52:53]
	v_cvt_pk_bf16_f32 v34, v34, v35
	v_sub_f32_e32 v8, v4, v5
	v_add_f32_e32 v4, v4, v5
	v_cndmask_b32_e64 v8, v4, v8, s[40:41]
	v_mov_b32_dpp v5, v51 row_half_mirror row_mask:0xf bank_mask:0xf bound_ctrl:1
	v_mov_b32_dpp v4, v50 row_half_mirror row_mask:0xf bank_mask:0xf bound_ctrl:1
	v_cvt_pk_bf16_f32 v35, v56, v57
	v_mov_b32_dpp v5, v5 quad_perm:[3,2,1,0] row_mask:0xf bank_mask:0xf bound_ctrl:1
	v_mov_b32_dpp v4, v4 quad_perm:[3,2,1,0] row_mask:0xf bank_mask:0xf bound_ctrl:1
	v_pk_mul_f32 v[4:5], v[6:7], v[4:5]
	s_nop 0
	v_pk_fma_f32 v[6:7], v[10:11], v[50:51], v[4:5] neg_lo:[0,0,1] neg_hi:[0,0,1]
	v_pk_fma_f32 v[4:5], v[10:11], v[50:51], v[4:5]
	v_mov_b64_e32 v[50:51], v[48:49]
	v_cndmask_b32_e64 v5, v5, v7, s[40:41]
	v_cndmask_b32_e64 v6, v4, v6, s[40:41]
	v_cvt_pk_bf16_f32 v5, v6, v5
	v_lshl_add_u64 v[6:7], s[2:3], 0, v[42:43]
	v_cvt_pk_bf16_f32 v4, v54, v8
	global_store_dwordx4 v[6:7], v[32:35], off nt
	v_lshl_add_u64 v[6:7], s[2:3], 0, v[40:41]
	v_lshl_add_u64 v[40:41], v[40:41], 0, s[4:5]
	v_lshl_add_u64 v[42:43], v[42:43], 0, s[4:5]
	s_mov_b64 s[4:5], 0xd00000
	global_store_dwordx2 v[6:7], v[4:5], off nt
	v_lshl_add_u64 v[44:45], v[44:45], 0, s[4:5]
	s_mov_b64 s[4:5], 0x700000
	v_mov_b64_e32 v[34:35], v[22:23]
	v_mov_b64_e32 v[8:9], v[28:29]
	v_mov_b64_e32 v[4:5], v[24:25]
	v_lshl_add_u64 v[46:47], v[46:47], 0, s[4:5]
	v_mov_b64_e32 v[32:33], v[20:21]
	v_mov_b64_e32 v[10:11], v[30:31]
	v_mov_b64_e32 v[6:7], v[26:27]
	s_cbranch_vccnz .LBB0_405

.LBB0_1165:
	v_mul_f32_e32 v50, v37, v37
	v_mul_f32_e32 v51, v35, v35
	v_fmac_f32_e32 v50, v36, v36
	v_fmac_f32_e32 v51, v34, v34
	v_add_f32_e32 v50, v50, v51
	v_mul_f32_e32 v51, v45, v45
	v_mul_f32_e32 v52, v43, v43
	v_fmac_f32_e32 v51, v44, v44
	v_fmac_f32_e32 v52, v42, v42
	v_add_f32_e32 v51, v51, v52
	v_add_f32_e32 v50, v50, v51
	v_mul_f32_e32 v51, v41, v41
	v_mul_f32_e32 v52, v39, v39
	v_fmac_f32_e32 v51, v40, v40
	v_fmac_f32_e32 v52, v38, v38
	v_add_f32_e32 v51, v51, v52
	v_add_f32_e32 v50, v51, v50
	v_mul_f32_e32 v51, v49, v49
	v_mul_f32_e32 v52, v47, v47
	v_fmac_f32_e32 v51, v48, v48
	v_fmac_f32_e32 v52, v46, v46
	v_add_f32_e32 v51, v51, v52
	v_add_f32_e32 v50, v51, v50
	s_addk_i32 s18, 0x800
	s_andn2_b64 vcc, exec, s[2:3]
	v_add_f32_dpp v50, v50, v50 quad_perm:[1,0,3,2] row_mask:0xf bank_mask:0xf bound_ctrl:1
	s_nop 1
	v_add_f32_dpp v50, v50, v50 quad_perm:[2,3,0,1] row_mask:0xf bank_mask:0xf bound_ctrl:1
	s_nop 1
	v_add_f32_dpp v50, v50, v50 row_half_mirror row_mask:0xf bank_mask:0xf bound_ctrl:1
	s_nop 1
	v_add_f32_dpp v50, v50, v50 row_mirror row_mask:0xf bank_mask:0xf bound_ctrl:1
	v_mov_b32_e32 v51, v50
	s_nop 1
	v_permlane16_swap_b32_e32 v50, v51
	v_add_f32_e32 v50, v50, v51
	v_mov_b32_e32 v51, v50
	s_nop 1
	v_permlane32_swap_b32_e32 v50, v51
	v_add_f32_e32 v50, v50, v51
	v_fmamk_f32 v50, v50, 0x3a800000, v240
	v_rsq_f32_e32 v50, v50
	s_nop 0
	v_pk_mul_f32 v[36:37], v[36:37], v[50:51] op_sel_hi:[1,0]
	v_pk_mul_f32 v[34:35], v[34:35], v[50:51] op_sel_hi:[1,0]
	v_pk_mul_f32 v[36:37], v[12:13], v[36:37]
	v_pk_mul_f32 v[34:35], v[14:15], v[34:35]
	v_cvt_pk_bf16_f32 v36, v36, v37
	v_cvt_pk_bf16_f32 v37, v34, v35
	global_store_dwordx2 v[32:33], v[36:37], off nt
	v_pk_mul_f32 v[34:35], v[44:45], v[50:51] op_sel_hi:[1,0]
	v_pk_mul_f32 v[36:37], v[42:43], v[50:51] op_sel_hi:[1,0]
	v_pk_mul_f32 v[34:35], v[8:9], v[34:35]
	v_pk_mul_f32 v[36:37], v[10:11], v[36:37]
	v_cvt_pk_bf16_f32 v34, v34, v35
	v_cvt_pk_bf16_f32 v35, v36, v37
	global_store_dwordx2 v[32:33], v[34:35], off offset:512 nt
	v_pk_mul_f32 v[34:35], v[40:41], v[50:51] op_sel_hi:[1,0]
	v_pk_mul_f32 v[36:37], v[38:39], v[50:51] op_sel_hi:[1,0]
	v_pk_mul_f32 v[34:35], v[4:5], v[34:35]
	v_pk_mul_f32 v[36:37], v[6:7], v[36:37]
	v_cvt_pk_bf16_f32 v34, v34, v35
	v_cvt_pk_bf16_f32 v35, v36, v37
	global_store_dwordx2 v[32:33], v[34:35], off offset:1024 nt
	v_pk_mul_f32 v[34:35], v[48:49], v[50:51] op_sel_hi:[1,0]
	v_pk_mul_f32 v[36:37], v[46:47], v[50:51] op_sel_hi:[1,0]
	v_pk_mul_f32 v[34:35], v[0:1], v[34:35]
	v_pk_mul_f32 v[36:37], v[2:3], v[36:37]
	v_cvt_pk_bf16_f32 v34, v34, v35
	v_cvt_pk_bf16_f32 v35, v36, v37
	global_store_dwordx2 v[32:33], v[34:35], off offset:1536 nt
	v_lshl_add_u64 v[32:33], v[32:33], 0, s[6:7]
	v_mov_b32_e32 v36, v16
	v_mov_b32_e32 v37, v17
	v_mov_b32_e32 v34, v18
	v_mov_b32_e32 v35, v19
	v_mov_b32_e32 v44, v20
	v_mov_b32_e32 v45, v21
	v_mov_b32_e32 v42, v22
	v_mov_b32_e32 v43, v23
	v_mov_b32_e32 v40, v24
	v_mov_b32_e32 v41, v25
	v_mov_b32_e32 v38, v26
	v_mov_b32_e32 v39, v27
	v_mov_b32_e32 v48, v28
	v_mov_b32_e32 v49, v29
	v_mov_b32_e32 v46, v30
	v_mov_b32_e32 v47, v31
	s_cbranch_vccz .LBB0_1168

.LBB0_1391:
	v_mul_f32_e32 v152, v173, v173
	v_mul_f32_e32 v153, v158, v158
	v_fmac_f32_e32 v152, v174, v174
	v_fmac_f32_e32 v153, v159, v159
	v_add_f32_e32 v152, v152, v153
	v_mul_f32_e32 v153, v171, v171
	v_mul_f32_e32 v154, v169, v169
	v_fmac_f32_e32 v153, v172, v172
	v_fmac_f32_e32 v154, v170, v170
	v_add_f32_e32 v153, v153, v154
	v_add_f32_e32 v152, v152, v153
	v_mul_f32_e32 v153, v167, v167
	v_mul_f32_e32 v154, v165, v165
	v_fmac_f32_e32 v153, v168, v168
	v_fmac_f32_e32 v154, v166, v166
	v_add_f32_e32 v153, v153, v154
	v_add_f32_e32 v152, v152, v153
	v_mul_f32_e32 v153, v163, v163
	v_mul_f32_e32 v154, v160, v160
	v_fmac_f32_e32 v153, v164, v164
	v_fmac_f32_e32 v154, v162, v162
	v_add_f32_e32 v153, v153, v154
	v_add_f32_e32 v152, v152, v153
	v_mov_b32_e32 v180, v161
	v_lshl_add_u64 v[150:151], s[34:35], 0, v[146:147]
	v_add_f32_dpp v152, v152, v152 quad_perm:[1,0,3,2] row_mask:0xf bank_mask:0xf bound_ctrl:1
	s_mov_b32 s2, 0x2400000
	v_add_co_u32_e32 v150, vcc, s2, v150
	v_add_f32_dpp v152, v152, v152 quad_perm:[2,3,0,1] row_mask:0xf bank_mask:0xf bound_ctrl:1
	s_nop 0
	v_addc_co_u32_e32 v151, vcc, 0, v151, vcc
	v_add_f32_dpp v152, v152, v152 row_half_mirror row_mask:0xf bank_mask:0xf bound_ctrl:1
	v_lshl_add_u64 v[176:177], s[34:35], 0, v[148:149]
	s_brev_b32 s2, 4
	v_add_f32_dpp v152, v152, v152 row_mirror row_mask:0xf bank_mask:0xf bound_ctrl:1
	v_mov_b32_e32 v153, v152
	s_nop 1
	v_permlane16_swap_b32_e32 v152, v153
	v_add_f32_e32 v152, v152, v153
	v_mov_b32_e32 v153, v152
	s_nop 1
	v_permlane32_swap_b32_e32 v152, v153
	v_add_f32_e32 v152, v152, v153
	v_fmamk_f32 v152, v152, 0x3a800000, v240
	v_rsq_f32_e32 v175, v152
	global_load_dwordx2 v[156:157], v[150:151], off offset:2048
	global_load_dwordx2 v[154:155], v[150:151], off offset:2560
	global_load_dwordx2 v[152:153], v[150:151], off offset:3072
	s_nop 0
	global_load_dwordx2 v[150:151], v[150:151], off offset:3584
	v_mov_b32_e32 v186, v161
	v_mul_f32_e32 v174, v175, v174
	v_mul_f32_e32 v173, v175, v173
	v_mul_f32_e32 v174, v140, v174
	v_mul_f32_e32 v173, v141, v173
	v_mul_f32_e32 v159, v175, v159
	v_mul_f32_e32 v178, v142, v159
	v_mul_f32_e32 v159, 0x41800000, v174
	v_mul_f32_e32 v179, 0x41800000, v173
	v_cvt_pk_fp8_f32 v180, v159, v179
	v_mul_f32_e32 v158, v175, v158
	v_mul_f32_e32 v179, v143, v158
	v_mul_f32_e32 v158, 0x41800000, v178
	v_mul_f32_e32 v159, 0x41800000, v179
	v_cvt_pk_fp8_f32 v180, v158, v159 op_sel:[0,0,1]
	v_add_co_u32_e32 v158, vcc, s2, v176
	v_mul_f32_e32 v172, v175, v172
	s_nop 0
	v_addc_co_u32_e32 v159, vcc, 0, v177, vcc
	v_mul_f32_e32 v171, v175, v171
	global_store_dword v[158:159], v180, off nt
	v_mul_f32_e32 v176, v173, v120
	v_mul_f32_e32 v177, v173, v121
	v_mul_f32_e32 v180, v173, v122
	v_mul_f32_e32 v181, v173, v123
	v_mul_f32_e32 v182, v173, v112
	v_mul_f32_e32 v183, v173, v113
	v_mul_f32_e32 v184, v173, v114
	v_mul_f32_e32 v173, v173, v115
	v_mul_f32_e32 v172, v136, v172
	v_mul_f32_e32 v171, v137, v171
	v_fmac_f32_e32 v176, v174, v116
	v_fmac_f32_e32 v177, v174, v117
	v_fmac_f32_e32 v180, v174, v118
	v_fmac_f32_e32 v181, v174, v119
	v_fmac_f32_e32 v182, v174, v108
	v_fmac_f32_e32 v183, v174, v109
	v_fmac_f32_e32 v184, v174, v110
	v_fmac_f32_e32 v173, v174, v111
	v_mul_f32_e32 v174, 0x41800000, v172
	v_mul_f32_e32 v185, 0x41800000, v171
	v_cvt_pk_fp8_f32 v186, v174, v185
	v_mul_f32_e32 v170, v175, v170
	v_mul_f32_e32 v169, v175, v169
	v_mul_f32_e32 v170, v138, v170
	v_mul_f32_e32 v169, v139, v169
	v_mul_f32_e32 v174, 0x41800000, v170
	v_mul_f32_e32 v185, 0x41800000, v169
	v_cvt_pk_fp8_f32 v186, v174, v185 op_sel:[0,0,1]
	v_mul_f32_e32 v174, v171, v84
	v_fmac_f32_e32 v176, v178, v128
	v_fmac_f32_e32 v174, v172, v80
	v_fmac_f32_e32 v176, v179, v124
	v_fmac_f32_e32 v174, v170, v92
	v_add_f32_e32 v176, 0, v176
	v_fmac_f32_e32 v174, v169, v88
	v_add_f32_e32 v174, v176, v174
	v_mul_f32_e32 v176, v171, v85
	v_fmac_f32_e32 v177, v178, v129
	v_fmac_f32_e32 v176, v172, v81
	v_fmac_f32_e32 v177, v179, v125
	v_fmac_f32_e32 v176, v170, v93
	v_add_f32_e32 v177, 0, v177
	v_fmac_f32_e32 v176, v169, v89
	v_add_f32_e32 v176, v177, v176
	v_mul_f32_e32 v177, v171, v86
	v_fmac_f32_e32 v180, v178, v130
	v_fmac_f32_e32 v177, v172, v82
	v_fmac_f32_e32 v180, v179, v126
	v_fmac_f32_e32 v177, v170, v94
	v_add_f32_e32 v180, 0, v180
	v_fmac_f32_e32 v181, v178, v131
	v_fmac_f32_e32 v182, v178, v100
	v_fmac_f32_e32 v183, v178, v101
	v_fmac_f32_e32 v184, v178, v102
	v_fmac_f32_e32 v173, v178, v103
	v_fmac_f32_e32 v177, v169, v90
	v_mul_f32_e32 v178, v171, v87
	v_fmac_f32_e32 v181, v179, v127
	v_fmac_f32_e32 v182, v179, v104
	v_fmac_f32_e32 v183, v179, v105
	v_fmac_f32_e32 v184, v179, v106
	v_fmac_f32_e32 v173, v179, v107
	v_add_f32_e32 v177, v180, v177
	v_fmac_f32_e32 v178, v172, v83
	v_mul_f32_e32 v179, v171, v76
	v_mul_f32_e32 v180, v171, v77
	v_fmac_f32_e32 v178, v170, v95
	v_fmac_f32_e32 v179, v172, v72
	v_fmac_f32_e32 v180, v172, v73
	v_add_f32_e32 v181, 0, v181
	v_fmac_f32_e32 v178, v169, v91
	v_fmac_f32_e32 v179, v170, v64
	v_fmac_f32_e32 v180, v170, v65
	v_mul_f32_e32 v168, v175, v168
	v_mul_f32_e32 v167, v175, v167
	v_add_f32_e32 v182, 0, v182
	v_add_f32_e32 v183, 0, v183
	v_add_f32_e32 v178, v181, v178
	v_fmac_f32_e32 v179, v169, v68
	v_fmac_f32_e32 v180, v169, v69
	v_mul_f32_e32 v181, v171, v78
	v_mul_f32_e32 v171, v171, v79
	v_mul_f32_e32 v168, v132, v168
	v_mul_f32_e32 v167, v133, v167
	v_add_f32_e32 v179, v182, v179
	v_add_f32_e32 v180, v183, v180
	v_fmac_f32_e32 v181, v172, v74
	v_fmac_f32_e32 v171, v172, v75
	v_mul_f32_e32 v172, 0x41800000, v168
	v_mul_f32_e32 v182, 0x41800000, v167
	v_mov_b32_e32 v183, v161
	v_cvt_pk_fp8_f32 v183, v172, v182
	v_mul_f32_e32 v166, v175, v166
	v_mul_f32_e32 v165, v175, v165
	v_mul_f32_e32 v166, v134, v166
	v_mul_f32_e32 v165, v135, v165
	v_fmac_f32_e32 v171, v170, v67
	v_add_f32_e32 v173, 0, v173
	v_fmac_f32_e32 v181, v170, v66
	v_mul_f32_e32 v172, 0x41800000, v166
	v_mul_f32_e32 v182, 0x41800000, v165
	v_fmac_f32_e32 v171, v169, v71
	v_fmac_f32_e32 v181, v169, v70
	v_cvt_pk_fp8_f32 v183, v172, v182 op_sel:[0,0,1]
	v_add_f32_e32 v169, v173, v171
	v_mul_f32_e32 v170, v167, v52
	v_mul_f32_e32 v171, v167, v53
	v_mul_f32_e32 v172, v167, v54
	v_fmac_f32_e32 v170, v168, v48
	v_fmac_f32_e32 v171, v168, v49
	v_fmac_f32_e32 v172, v168, v50
	v_mul_f32_e32 v173, v167, v55
	v_fmac_f32_e32 v170, v166, v60
	v_fmac_f32_e32 v171, v166, v61
	v_fmac_f32_e32 v172, v166, v62
	v_fmac_f32_e32 v173, v168, v51
	v_fmac_f32_e32 v170, v165, v56
	v_fmac_f32_e32 v171, v165, v57
	v_fmac_f32_e32 v172, v165, v58
	v_fmac_f32_e32 v173, v166, v63
	v_mul_f32_e32 v164, v175, v164
	v_mul_f32_e32 v163, v175, v163
	v_add_f32_e32 v170, v174, v170
	v_add_f32_e32 v171, v176, v171
	v_add_f32_e32 v172, v177, v172
	v_fmac_f32_e32 v173, v165, v59
	v_mul_f32_e32 v174, v167, v44
	v_mul_f32_e32 v176, v167, v45
	v_mul_f32_e32 v177, v167, v46
	v_mul_f32_e32 v167, v167, v47
	v_mul_f32_e32 v164, v96, v164
	v_mul_f32_e32 v163, v97, v163
	v_add_f32_e32 v173, v178, v173
	v_fmac_f32_e32 v174, v168, v40
	v_fmac_f32_e32 v176, v168, v41
	v_fmac_f32_e32 v177, v168, v42
	v_fmac_f32_e32 v167, v168, v43
	v_mul_f32_e32 v162, v175, v162
	v_mul_f32_e32 v160, v175, v160
	v_mul_f32_e32 v168, 0x41800000, v164
	v_mul_f32_e32 v175, 0x41800000, v163
	v_mov_b32_e32 v178, v161
	v_cvt_pk_fp8_f32 v178, v168, v175
	v_mul_f32_e32 v162, v98, v162
	v_mul_f32_e32 v160, v99, v160
	v_mul_f32_e32 v168, 0x41800000, v162
	v_mul_f32_e32 v175, 0x41800000, v160
	v_cvt_pk_fp8_f32 v178, v168, v175 op_sel:[0,0,1]
	global_store_dword v[158:159], v186, off offset:256 nt
	global_store_dword v[158:159], v183, off offset:512 nt
	v_fmac_f32_e32 v174, v166, v32
	global_store_dword v[158:159], v178, off offset:768 nt
	v_mul_f32_e32 v159, v163, v21
	v_fmac_f32_e32 v159, v164, v17
	v_fmac_f32_e32 v159, v162, v29
	v_fmac_f32_e32 v159, v160, v25
	v_fmac_f32_e32 v176, v166, v33
	v_fmac_f32_e32 v177, v166, v34
	v_fmac_f32_e32 v167, v166, v35
	v_add_f32_e32 v166, v171, v159
	v_mul_f32_e32 v159, v163, v22
	v_fmac_f32_e32 v159, v164, v18
	v_fmac_f32_e32 v159, v162, v30
	v_fmac_f32_e32 v167, v165, v39
	v_fmac_f32_e32 v159, v160, v26
	v_fmac_f32_e32 v174, v165, v36
	v_fmac_f32_e32 v176, v165, v37
	v_fmac_f32_e32 v177, v165, v38
	v_add_f32_e32 v165, v169, v167
	v_add_f32_e32 v167, v172, v159
	v_mul_f32_e32 v159, v163, v23
	v_fmac_f32_e32 v159, v164, v19
	v_fmac_f32_e32 v159, v162, v31
	v_fmac_f32_e32 v159, v160, v27
	v_add_f32_e32 v168, v173, v159
	v_mul_f32_e32 v159, v163, v4
	v_fmac_f32_e32 v159, v164, v0
	v_fmac_f32_e32 v159, v162, v12
	v_add_f32_e32 v174, v179, v174
	v_fmac_f32_e32 v159, v160, v8
	v_mul_f32_e32 v158, v163, v20
	v_add_f32_e32 v169, v174, v159
	v_mul_f32_e32 v159, v163, v5
	v_fmac_f32_e32 v158, v164, v16
	v_fmac_f32_e32 v159, v164, v1
	v_fmac_f32_e32 v158, v162, v28
	v_fmac_f32_e32 v159, v162, v13
	v_add_f32_e32 v176, v180, v176
	v_fmac_f32_e32 v158, v160, v24
	v_fmac_f32_e32 v159, v160, v9
	v_add_f32_e32 v158, v170, v158
	v_add_f32_e32 v170, v176, v159
	v_mul_f32_e32 v159, v163, v6
	v_add_f32_e32 v184, 0, v184
	v_fmac_f32_e32 v159, v164, v2
	v_add_f32_e32 v181, v184, v181
	v_fmac_f32_e32 v159, v162, v14
	v_add_f32_e32 v177, v181, v177
	v_fmac_f32_e32 v159, v160, v10
	v_add_f32_e32 v171, v177, v159
	v_mul_f32_e32 v159, v163, v7
	v_add_f32_dpp v158, v158, v158 quad_perm:[1,0,3,2] row_mask:0xf bank_mask:0xf bound_ctrl:1
	v_fmac_f32_e32 v159, v164, v3
	v_fmac_f32_e32 v159, v162, v15
	v_add_f32_dpp v158, v158, v158 quad_perm:[2,3,0,1] row_mask:0xf bank_mask:0xf bound_ctrl:1
	v_fmac_f32_e32 v159, v160, v11
	v_add_f32_e32 v173, v165, v159
	v_add_f32_dpp v158, v158, v158 row_half_mirror row_mask:0xf bank_mask:0xf bound_ctrl:1
	v_add_f32_dpp v165, v168, v168 quad_perm:[1,0,3,2] row_mask:0xf bank_mask:0xf bound_ctrl:1
	v_add_f32_dpp v171, v171, v171 quad_perm:[1,0,3,2] row_mask:0xf bank_mask:0xf bound_ctrl:1
	v_add_f32_dpp v158, v158, v158 row_mirror row_mask:0xf bank_mask:0xf bound_ctrl:1
	v_mov_b32_e32 v159, v158
	s_nop 1
	v_permlane16_swap_b32_e32 v158, v159
	v_add_f32_e32 v159, v158, v159
	s_nop 0
	v_add_f32_dpp v158, v166, v166 quad_perm:[1,0,3,2] row_mask:0xf bank_mask:0xf bound_ctrl:1
	v_add_f32_dpp v173, v173, v173 quad_perm:[1,0,3,2] row_mask:0xf bank_mask:0xf bound_ctrl:1
	v_add_f32_dpp v165, v165, v165 quad_perm:[2,3,0,1] row_mask:0xf bank_mask:0xf bound_ctrl:1
	v_add_f32_dpp v158, v158, v158 quad_perm:[2,3,0,1] row_mask:0xf bank_mask:0xf bound_ctrl:1
	v_add_f32_dpp v171, v171, v171 quad_perm:[2,3,0,1] row_mask:0xf bank_mask:0xf bound_ctrl:1
	v_add_f32_dpp v173, v173, v173 quad_perm:[2,3,0,1] row_mask:0xf bank_mask:0xf bound_ctrl:1
	v_add_f32_dpp v158, v158, v158 row_half_mirror row_mask:0xf bank_mask:0xf bound_ctrl:1
	v_add_f32_dpp v165, v165, v165 row_half_mirror row_mask:0xf bank_mask:0xf bound_ctrl:1
	v_add_f32_dpp v171, v171, v171 row_half_mirror row_mask:0xf bank_mask:0xf bound_ctrl:1
	v_add_f32_dpp v158, v158, v158 row_mirror row_mask:0xf bank_mask:0xf bound_ctrl:1
	v_mov_b32_e32 v160, v158
	s_nop 1
	v_permlane16_swap_b32_e32 v158, v160
	v_add_f32_e32 v158, v158, v160
	s_nop 0
	v_add_f32_dpp v160, v167, v167 quad_perm:[1,0,3,2] row_mask:0xf bank_mask:0xf bound_ctrl:1
	v_add_f32_dpp v167, v169, v169 quad_perm:[1,0,3,2] row_mask:0xf bank_mask:0xf bound_ctrl:1
	v_add_f32_dpp v169, v170, v170 quad_perm:[1,0,3,2] row_mask:0xf bank_mask:0xf bound_ctrl:1
	v_add_f32_dpp v160, v160, v160 quad_perm:[2,3,0,1] row_mask:0xf bank_mask:0xf bound_ctrl:1
	v_add_f32_dpp v167, v167, v167 quad_perm:[2,3,0,1] row_mask:0xf bank_mask:0xf bound_ctrl:1
	v_add_f32_dpp v169, v169, v169 quad_perm:[2,3,0,1] row_mask:0xf bank_mask:0xf bound_ctrl:1
	v_add_f32_dpp v160, v160, v160 row_half_mirror row_mask:0xf bank_mask:0xf bound_ctrl:1
	v_add_f32_dpp v167, v167, v167 row_half_mirror row_mask:0xf bank_mask:0xf bound_ctrl:1
	v_add_f32_dpp v169, v169, v169 row_half_mirror row_mask:0xf bank_mask:0xf bound_ctrl:1
	v_add_f32_dpp v173, v173, v173 row_half_mirror row_mask:0xf bank_mask:0xf bound_ctrl:1
	v_add_f32_dpp v160, v160, v160 row_mirror row_mask:0xf bank_mask:0xf bound_ctrl:1
	v_add_f32_dpp v165, v165, v165 row_mirror row_mask:0xf bank_mask:0xf bound_ctrl:1
	v_add_f32_dpp v167, v167, v167 row_mirror row_mask:0xf bank_mask:0xf bound_ctrl:1
	v_add_f32_dpp v169, v169, v169 row_mirror row_mask:0xf bank_mask:0xf bound_ctrl:1
	v_add_f32_dpp v171, v171, v171 row_mirror row_mask:0xf bank_mask:0xf bound_ctrl:1
	v_add_f32_dpp v173, v173, v173 row_mirror row_mask:0xf bank_mask:0xf bound_ctrl:1
	v_mov_b32_e32 v164, v160
	v_mov_b32_e32 v166, v165
	v_mov_b32_e32 v168, v167
	v_mov_b32_e32 v170, v169
	v_mov_b32_e32 v172, v171
	v_mov_b32_e32 v174, v173
	v_permlane16_swap_b32_e32 v160, v164
	v_permlane16_swap_b32_e32 v165, v166
	v_permlane16_swap_b32_e32 v167, v168
	v_permlane16_swap_b32_e32 v169, v170
	v_permlane16_swap_b32_e32 v171, v172
	v_permlane16_swap_b32_e32 v173, v174
	v_add_f32_e32 v160, v160, v164
	v_add_f32_e32 v165, v165, v166
	v_add_f32_e32 v167, v167, v168
	v_add_f32_e32 v169, v169, v170
	v_add_f32_e32 v171, v171, v172
	v_add_f32_e32 v173, v173, v174
	v_mov_b32_e32 v163, v159
	v_mov_b32_e32 v162, v158
	v_mov_b32_e32 v164, v160
	v_mov_b32_e32 v166, v165
	v_mov_b32_e32 v168, v167
	v_mov_b32_e32 v170, v169
	v_mov_b32_e32 v172, v171
	v_mov_b32_e32 v174, v173
	v_permlane32_swap_b32_e32 v159, v163
	v_permlane32_swap_b32_e32 v158, v162
	v_permlane32_swap_b32_e32 v160, v164
	v_permlane32_swap_b32_e32 v165, v166
	v_permlane32_swap_b32_e32 v167, v168
	v_permlane32_swap_b32_e32 v169, v170
	v_permlane32_swap_b32_e32 v171, v172
	v_permlane32_swap_b32_e32 v173, v174
	s_and_saveexec_b64 s[2:3], s[36:37]
	s_cbranch_execz .LBB0_1390
	v_pk_add_f32 v[158:159], v[158:159], v[162:163]
	v_add_f32_e32 v160, v160, v164
	v_cmp_gt_f32_e32 vcc, v158, v159
	v_add_f32_e32 v165, v165, v166
	v_add_f32_e32 v167, v167, v168
	v_cndmask_b32_e32 v162, v159, v158, vcc
	v_cmp_gt_f32_e64 s[38:39], v160, v162
	v_add_f32_e32 v169, v169, v170
	v_cndmask_b32_e64 v163, 0, 1, vcc
	v_cndmask_b32_e64 v162, v162, v160, s[38:39]
	v_cmp_gt_f32_e64 s[40:41], v165, v162
	v_cndmask_b32_e64 v163, v163, 2, s[38:39]
	v_add_f32_e32 v171, v171, v172
	v_cndmask_b32_e64 v162, v162, v165, s[40:41]
	v_cmp_gt_f32_e64 s[42:43], v167, v162
	v_cndmask_b32_e64 v163, v163, 3, s[40:41]
	v_add_f32_e32 v173, v173, v174
	v_cndmask_b32_e64 v162, v162, v167, s[42:43]
	v_cmp_gt_f32_e64 s[44:45], v169, v162
	v_cndmask_b32_e64 v163, v163, 4, s[42:43]
	s_mov_b32 s31, 0xff61b1e6
	v_cndmask_b32_e64 v162, v162, v169, s[44:45]
	v_cmp_gt_f32_e64 s[46:47], v171, v162
	v_cndmask_b32_e64 v163, v163, 5, s[44:45]
	v_cmp_nlt_f32_e64 s[50:51], s31, v159
	v_cndmask_b32_e64 v162, v162, v171, s[46:47]
	v_cndmask_b32_e64 v163, v163, 6, s[46:47]
	v_cmp_ngt_f32_e32 vcc, v173, v162
	v_mov_b32_e32 v164, 0xff61b1e6
	s_and_b64 s[22:23], vcc, s[46:47]
	v_cndmask_b32_e32 v163, 7, v163, vcc
	v_cmp_eq_u32_e64 s[48:49], 0, v163
	s_or_b64 s[48:49], s[48:49], s[50:51]
	v_cmp_ne_u32_e64 s[46:47], 1, v163
	v_cndmask_b32_e64 v159, v159, v164, s[48:49]
	v_cmp_gt_f32_e64 s[50:51], v158, v159
	s_and_b64 s[46:47], s[46:47], s[50:51]
	v_cndmask_b32_e64 v158, v159, v158, s[46:47]
	v_cmp_ne_u32_e64 s[44:45], 2, v163
	v_cmp_gt_f32_e64 s[50:51], v160, v158
	s_and_b64 s[44:45], s[44:45], s[50:51]
	v_cndmask_b32_e64 v158, v158, v160, s[44:45]
	v_cmp_ne_u32_e64 s[42:43], 3, v163
	v_cmp_gt_f32_e64 s[50:51], v165, v158
	s_and_b64 s[42:43], s[42:43], s[50:51]
	v_cndmask_b32_e64 v158, v158, v165, s[42:43]
	v_cmp_ne_u32_e64 s[40:41], 4, v163
	v_cmp_gt_f32_e64 s[50:51], v167, v158
	s_and_b64 s[40:41], s[40:41], s[50:51]
	v_cndmask_b32_e64 v158, v158, v167, s[40:41]
	v_cmp_ne_u32_e64 s[38:39], 5, v163
	v_cmp_gt_f32_e64 s[50:51], v169, v158
	s_and_b64 s[38:39], s[38:39], s[50:51]
	v_cndmask_b32_e64 v158, v158, v169, s[38:39]
	v_cndmask_b32_e64 v159, 0, -1, s[48:49]
	v_cmp_ngt_f32_e64 s[50:51], v171, v158
	v_cndmask_b32_e64 v159, v159, 1, s[46:47]
	s_or_b64 s[50:51], s[22:23], s[50:51]
	v_cndmask_b32_e64 v159, v159, 2, s[44:45]
	v_cndmask_b32_e64 v158, v171, v158, s[50:51]
	v_cndmask_b32_e64 v159, v159, 3, s[42:43]
	v_cmp_gt_f32_e64 s[54:55], v173, v158
	v_cndmask_b32_e64 v159, v159, 4, s[40:41]
	v_cndmask_b32_e64 v159, v159, 5, s[38:39]
	s_and_b64 s[38:39], vcc, s[54:55]
	v_cndmask_b32_e64 v158, v158, v173, s[38:39]
	v_cndmask_b32_e32 v160, v173, v162, vcc
	v_sub_f32_e32 v158, v158, v160
	v_mul_f32_e32 v160, 0x3fb8aa3b, v158
	s_mov_b32 s22, 0x3fb8aa3b
	v_fma_f32 v162, v158, s22, -v160
	v_rndne_f32_e32 v164, v160
	v_fmac_f32_e32 v162, 0x32a5705f, v158
	v_sub_f32_e32 v160, v160, v164
	v_add_f32_e32 v160, v160, v162
	v_exp_f32_e32 v160, v160
	v_cvt_i32_f32_e32 v162, v164
	s_mov_b32 s22, 0xc2ce8ed0
	v_cmp_ngt_f32_e32 vcc, s22, v158
	s_mov_b32 s22, 0x42b17218
	v_ldexp_f32 v160, v160, v162
	v_cndmask_b32_e32 v160, 0, v160, vcc
	v_cmp_nlt_f32_e32 vcc, s22, v158
	s_add_i32 s22, s19, s7
	s_add_i32 s23, s22, 0x20800
	v_cndmask_b32_e32 v158, v242, v160, vcc
	v_add_f32_e32 v160, 1.0, v158
	v_mov_b32_e32 v162, s23
	s_add_i32 s22, s22, 0x20804
	ds_write_b32 v162, v163
	v_mov_b32_e32 v162, s22
	v_div_scale_f32 v163, s[22:23], v160, v160, v158
	v_rcp_f32_e32 v164, v163
	v_cndmask_b32_e64 v159, 6, v159, s[50:51]
	v_cndmask_b32_e64 v159, v159, 7, s[38:39]
	ds_write_b32 v162, v159
	v_fma_f32 v159, -v163, v164, 1.0
	v_fmac_f32_e32 v164, v159, v164
	v_div_scale_f32 v159, vcc, v158, v160, v158
	v_mul_f32_e32 v162, v159, v164
	v_fma_f32 v165, -v163, v162, v159
	v_fmac_f32_e32 v162, v165, v164
	v_fma_f32 v159, -v163, v162, v159
	v_div_scale_f32 v163, s[38:39], v160, v160, 1.0
	v_rcp_f32_e32 v165, v163
	v_div_fmas_f32 v159, v159, v164, v162
	v_div_fixup_f32 v159, v159, v160, v158
	s_add_u32 s22, s34, s11
	v_fma_f32 v158, -v163, v165, 1.0
	v_fmac_f32_e32 v165, v158, v165
	v_div_scale_f32 v158, vcc, 1.0, v160, 1.0
	v_mul_f32_e32 v162, v158, v165
	v_fma_f32 v164, -v163, v162, v158
	v_fmac_f32_e32 v162, v164, v165
	v_fma_f32 v158, -v163, v162, v158
	v_div_fmas_f32 v158, v158, v165, v162
	s_addc_u32 s23, s35, s18
	v_div_fixup_f32 v158, v158, v160, 1.0
	global_store_dwordx2 v161, v[158:159], s[22:23] nt
	s_branch .LBB0_1390

.LBB0_1461:
	s_or_b64 exec, exec, s[18:19]
	v_ashrrev_i32_e32 v1, 31, v0
	v_lshl_add_u64 v[0:1], v[0:1], 4, s[2:3]
	s_mov_b64 s[2:3], 0x20000000
	v_lshl_add_u64 v[14:15], v[0:1], 0, s[2:3]
	s_mov_b64 s[2:3], 0xb800000
	v_lshl_add_u64 v[12:13], v[0:1], 0, s[2:3]
	s_lshl_b32 s3, s7, 7
	s_add_i32 s2, 0, 0x20800
	s_add_i32 s3, s2, s3
	v_mov_b32_e32 v4, s3
	s_waitcnt lgkmcnt(0)
	s_waitcnt lgkmcnt(0)
	s_barrier
	ds_read_b32 v0, v4
	s_lshl_b32 s3, s7, 4
	v_readlane_b32 s18, v253, 44
	s_add_i32 s10, s3, s18
	s_ashr_i32 s11, s10, 31
	s_waitcnt lgkmcnt(0)
	v_lshlrev_b32_e32 v0, 2, v0
	v_add_u32_e32 v0, s2, v0
	ds_read_b32 v1, v0 offset:2144
	ds_read_b32 v0, v0 offset:2112
	s_lshl_b64 s[10:11], s[10:11], 10
	s_lshl_b32 s6, s7, 5
	s_or_b32 s3, s6, 2
	s_lshl_b32 s7, s3, 2
	s_waitcnt lgkmcnt(0)
	v_add_u32_e32 v0, v0, v1
	ds_read_b32 v1, v4 offset:1024
	s_add_i32 s7, s2, s7
	s_ashr_i32 s3, s3, 1
	s_waitcnt lgkmcnt(0)
	v_add_u32_e32 v16, v0, v1
	v_lshl_add_u64 v[0:1], v[14:15], 0, s[10:11]
	global_load_dwordx4 v[0:3], v[0:1], off
	ds_read_b32 v5, v4 offset:4
	s_add_i32 s10, s3, s18
	s_or_b32 s3, s6, 3
	s_ashr_i32 s11, s10, 31
	s_lshl_b64 s[10:11], s[10:11], 10
	s_waitcnt lgkmcnt(0)
	v_lshlrev_b32_e32 v5, 2, v5
	v_add_u32_e32 v5, s2, v5
	ds_read_b32 v6, v5 offset:2144
	ds_read_b32 v5, v5 offset:2112
	ds_read_b32 v4, v4 offset:1028
	v_ashrrev_i32_e32 v17, 31, v16
	v_lshlrev_b64 v[16:17], 10, v[16:17]
	v_lshl_add_u64 v[16:17], v[12:13], 0, v[16:17]
	s_waitcnt lgkmcnt(1)
	v_add_u32_e32 v5, v5, v6
	s_waitcnt lgkmcnt(0)
	v_add_u32_e32 v18, v5, v4
	v_mov_b32_e32 v4, s7
	ds_read_b32 v5, v4
	s_lshl_b32 s7, s3, 2
	s_add_i32 s7, s2, s7
	v_mov_b32_e32 v8, s7
	s_ashr_i32 s3, s3, 1
	s_waitcnt lgkmcnt(0)
	v_lshlrev_b32_e32 v5, 2, v5
	v_add_u32_e32 v5, s2, v5
	ds_read_b32 v6, v5 offset:2144
	ds_read_b32 v5, v5 offset:2112
	ds_read_b32 v4, v4 offset:1024
	v_ashrrev_i32_e32 v19, 31, v18
	s_waitcnt lgkmcnt(1)
	v_add_u32_e32 v5, v5, v6
	s_waitcnt lgkmcnt(0)
	v_add_u32_e32 v20, v5, v4
	v_lshl_add_u64 v[4:5], v[14:15], 0, s[10:11]
	global_load_dwordx4 v[4:7], v[4:5], off
	ds_read_b32 v9, v8
	s_add_i32 s10, s3, s18
	s_ashr_i32 s11, s10, 31
	s_lshl_b64 s[10:11], s[10:11], 10
	v_ashrrev_i32_e32 v21, 31, v20
	s_waitcnt lgkmcnt(0)
	v_lshlrev_b32_e32 v9, 2, v9
	v_add_u32_e32 v9, s2, v9
	ds_read_b32 v10, v9 offset:2144
	ds_read_b32 v9, v9 offset:2112
	ds_read_b32 v8, v8 offset:1024
	s_or_b32 s3, s6, 4
	s_lshl_b32 s7, s3, 2
	s_add_i32 s7, s2, s7
	s_waitcnt lgkmcnt(1)
	v_add_u32_e32 v9, v9, v10
	s_waitcnt lgkmcnt(0)
	v_add_u32_e32 v22, v9, v8
	v_lshl_add_u64 v[8:9], v[14:15], 0, s[10:11]
	global_load_dwordx4 v[8:11], v[8:9], off
	v_ashrrev_i32_e32 v23, 31, v22
	s_ashr_i32 s3, s3, 1
	s_add_i32 s10, s3, s18
	s_or_b32 s3, s6, 5
	s_ashr_i32 s11, s10, 31
	s_lshl_b64 s[10:11], s[10:11], 10
	s_waitcnt vmcnt(2)
	global_store_dwordx4 v[16:17], v[0:3], off nt
	v_lshlrev_b64 v[16:17], 10, v[18:19]
	v_lshl_add_u64 v[16:17], v[12:13], 0, v[16:17]
	global_store_dwordx4 v[16:17], v[0:3], off nt
	s_nop 1
	v_lshlrev_b64 v[0:1], 10, v[20:21]
	v_lshl_add_u64 v[0:1], v[12:13], 0, v[0:1]
	s_waitcnt vmcnt(3)
	global_store_dwordx4 v[0:1], v[4:7], off nt
	v_lshlrev_b64 v[0:1], 10, v[22:23]
	v_lshl_add_u64 v[0:1], v[12:13], 0, v[0:1]
	s_waitcnt vmcnt(3)
	global_store_dwordx4 v[0:1], v[8:11], off nt
	v_mov_b32_e32 v0, s7
	ds_read_b32 v1, v0
	s_lshl_b32 s7, s3, 2
	s_add_i32 s7, s2, s7
	v_mov_b32_e32 v4, s7
	s_ashr_i32 s3, s3, 1
	s_waitcnt lgkmcnt(0)
	v_lshlrev_b32_e32 v1, 2, v1
	v_add_u32_e32 v1, s2, v1
	ds_read_b32 v2, v1 offset:2144
	ds_read_b32 v1, v1 offset:2112
	ds_read_b32 v0, v0 offset:1024
	s_waitcnt lgkmcnt(1)
	v_add_u32_e32 v1, v1, v2
	s_waitcnt lgkmcnt(0)
	v_add_u32_e32 v8, v1, v0
	v_lshl_add_u64 v[0:1], v[14:15], 0, s[10:11]
	global_load_dwordx4 v[0:3], v[0:1], off
	ds_read_b32 v5, v4
	s_add_i32 s10, s3, s18
	s_or_b32 s3, s6, 6
	s_ashr_i32 s11, s10, 31
	s_lshl_b32 s7, s3, 2
	s_waitcnt lgkmcnt(0)
	v_lshlrev_b32_e32 v5, 2, v5
	v_add_u32_e32 v5, s2, v5
	ds_read_b32 v6, v5 offset:2144
	ds_read_b32 v5, v5 offset:2112
	ds_read_b32 v4, v4 offset:1024
	s_lshl_b64 s[10:11], s[10:11], 10
	s_add_i32 s7, s2, s7
	v_mov_b32_e32 v9, s7
	s_waitcnt lgkmcnt(1)
	v_add_u32_e32 v5, v5, v6
	s_waitcnt lgkmcnt(0)
	v_add_u32_e32 v10, v5, v4
	v_lshl_add_u64 v[4:5], v[14:15], 0, s[10:11]
	global_load_dwordx4 v[4:7], v[4:5], off
	ds_read_b32 v11, v9
	s_ashr_i32 s3, s3, 1
	s_add_i32 s10, s3, s18
	s_or_b32 s3, s6, 7
	s_ashr_i32 s11, s10, 31
	s_waitcnt lgkmcnt(0)
	v_lshlrev_b32_e32 v11, 2, v11
	v_add_u32_e32 v11, s2, v11
	ds_read_b32 v16, v11 offset:2144
	ds_read_b32 v11, v11 offset:2112
	ds_read_b32 v9, v9 offset:1024
	s_lshl_b32 s7, s3, 2
	s_lshl_b64 s[10:11], s[10:11], 10
	s_add_i32 s7, s2, s7
	s_waitcnt lgkmcnt(1)
	v_add_u32_e32 v11, v11, v16
	s_waitcnt lgkmcnt(0)
	v_add_u32_e32 v16, v11, v9
	v_lshl_add_u64 v[18:19], v[14:15], 0, s[10:11]
	v_mov_b32_e32 v9, s7
	global_load_dwordx4 v[18:21], v[18:19], off
	ds_read_b32 v11, v9
	s_ashr_i32 s3, s3, 1
	s_add_i32 s10, s3, s18
	s_ashr_i32 s11, s10, 31
	s_lshl_b64 s[10:11], s[10:11], 10
	s_waitcnt lgkmcnt(0)
	v_lshlrev_b32_e32 v11, 2, v11
	v_add_u32_e32 v11, s2, v11
	v_lshl_add_u64 v[22:23], v[14:15], 0, s[10:11]
	ds_read_b32 v17, v11 offset:2144
	ds_read_b32 v11, v11 offset:2112
	ds_read_b32 v9, v9 offset:1024
	global_load_dwordx4 v[22:25], v[22:23], off
	s_or_b32 s3, s6, 8
	s_lshl_b32 s7, s3, 2
	s_waitcnt lgkmcnt(1)
	v_add_u32_e32 v11, v11, v17
	s_waitcnt lgkmcnt(0)
	v_add_u32_e32 v26, v11, v9
	v_ashrrev_i32_e32 v9, 31, v8
	v_lshlrev_b64 v[8:9], 10, v[8:9]
	v_lshl_add_u64 v[8:9], v[12:13], 0, v[8:9]
	v_ashrrev_i32_e32 v11, 31, v10
	v_ashrrev_i32_e32 v17, 31, v16
	v_ashrrev_i32_e32 v27, 31, v26
	s_add_i32 s7, s2, s7
	s_ashr_i32 s3, s3, 1
	s_add_i32 s10, s3, s18
	s_or_b32 s3, s6, 9
	s_ashr_i32 s11, s10, 31
	s_lshl_b64 s[10:11], s[10:11], 10
	s_waitcnt vmcnt(3)
	global_store_dwordx4 v[8:9], v[0:3], off nt
	s_nop 1
	v_lshlrev_b64 v[0:1], 10, v[10:11]
	v_lshl_add_u64 v[0:1], v[12:13], 0, v[0:1]
	s_waitcnt vmcnt(3)
	global_store_dwordx4 v[0:1], v[4:7], off nt
	v_lshlrev_b64 v[0:1], 10, v[16:17]
	v_lshl_add_u64 v[0:1], v[12:13], 0, v[0:1]
	s_waitcnt vmcnt(3)
	global_store_dwordx4 v[0:1], v[18:21], off nt
	v_lshlrev_b64 v[0:1], 10, v[26:27]
	v_lshl_add_u64 v[0:1], v[12:13], 0, v[0:1]
	s_waitcnt vmcnt(3)
	global_store_dwordx4 v[0:1], v[22:25], off nt
	v_mov_b32_e32 v0, s7
	ds_read_b32 v1, v0
	s_lshl_b32 s7, s3, 2
	s_add_i32 s7, s2, s7
	v_mov_b32_e32 v4, s7
	s_ashr_i32 s3, s3, 1
	s_waitcnt lgkmcnt(0)
	v_lshlrev_b32_e32 v1, 2, v1
	v_add_u32_e32 v1, s2, v1
	ds_read_b32 v2, v1 offset:2144
	ds_read_b32 v1, v1 offset:2112
	ds_read_b32 v0, v0 offset:1024
	s_waitcnt lgkmcnt(1)
	v_add_u32_e32 v1, v1, v2
	s_waitcnt lgkmcnt(0)
	v_add_u32_e32 v16, v1, v0
	v_lshl_add_u64 v[0:1], v[14:15], 0, s[10:11]
	global_load_dwordx4 v[0:3], v[0:1], off
	ds_read_b32 v5, v4
	s_add_i32 s10, s3, s18
	s_or_b32 s3, s6, 10
	s_ashr_i32 s11, s10, 31
	s_lshl_b32 s7, s3, 2
	s_waitcnt lgkmcnt(0)
	v_lshlrev_b32_e32 v5, 2, v5
	v_add_u32_e32 v5, s2, v5
	ds_read_b32 v6, v5 offset:2144
	ds_read_b32 v5, v5 offset:2112
	ds_read_b32 v4, v4 offset:1024
	s_lshl_b64 s[10:11], s[10:11], 10
	s_add_i32 s7, s2, s7
	v_mov_b32_e32 v8, s7
	s_waitcnt lgkmcnt(1)
	v_add_u32_e32 v5, v5, v6
	s_waitcnt lgkmcnt(0)
	v_add_u32_e32 v18, v5, v4
	v_lshl_add_u64 v[4:5], v[14:15], 0, s[10:11]
	global_load_dwordx4 v[4:7], v[4:5], off
	ds_read_b32 v9, v8
	s_ashr_i32 s3, s3, 1
	s_add_i32 s10, s3, s18
	s_or_b32 s3, s6, 11
	s_ashr_i32 s11, s10, 31
	s_waitcnt lgkmcnt(0)
	v_lshlrev_b32_e32 v9, 2, v9
	v_add_u32_e32 v9, s2, v9
	ds_read_b32 v10, v9 offset:2144
	ds_read_b32 v9, v9 offset:2112
	ds_read_b32 v8, v8 offset:1024
	s_lshl_b32 s7, s3, 2
	s_lshl_b64 s[10:11], s[10:11], 10
	s_add_i32 s7, s2, s7
	s_waitcnt lgkmcnt(1)
	v_add_u32_e32 v9, v9, v10
	s_waitcnt lgkmcnt(0)
	v_add_u32_e32 v20, v9, v8
	v_lshl_add_u64 v[8:9], v[14:15], 0, s[10:11]
	v_mov_b32_e32 v17, s7
	global_load_dwordx4 v[8:11], v[8:9], off
	ds_read_b32 v19, v17
	s_ashr_i32 s3, s3, 1
	s_add_i32 s10, s3, s18
	s_ashr_i32 s11, s10, 31
	s_lshl_b64 s[10:11], s[10:11], 10
	s_waitcnt lgkmcnt(0)
	v_lshlrev_b32_e32 v19, 2, v19
	v_add_u32_e32 v19, s2, v19
	v_lshl_add_u64 v[24:25], v[14:15], 0, s[10:11]
	ds_read_b32 v21, v19 offset:2144
	ds_read_b32 v19, v19 offset:2112
	ds_read_b32 v17, v17 offset:1024
	global_load_dwordx4 v[24:27], v[24:25], off
	s_or_b32 s3, s6, 12
	s_lshl_b32 s7, s3, 2
	s_waitcnt lgkmcnt(1)
	v_add_u32_e32 v19, v19, v21
	s_waitcnt lgkmcnt(0)
	v_add_u32_e32 v22, v19, v17
	v_ashrrev_i32_e32 v17, 31, v16
	v_lshlrev_b64 v[16:17], 10, v[16:17]
	v_lshl_add_u64 v[16:17], v[12:13], 0, v[16:17]
	v_ashrrev_i32_e32 v19, 31, v18
	v_ashrrev_i32_e32 v21, 31, v20
	v_ashrrev_i32_e32 v23, 31, v22
	s_add_i32 s7, s2, s7
	s_ashr_i32 s3, s3, 1
	s_add_i32 s10, s3, s18
	s_or_b32 s3, s6, 13
	s_ashr_i32 s11, s10, 31
	s_lshl_b64 s[10:11], s[10:11], 10
	s_waitcnt vmcnt(3)
	global_store_dwordx4 v[16:17], v[0:3], off nt
	s_nop 1
	v_lshlrev_b64 v[0:1], 10, v[18:19]
	v_lshl_add_u64 v[0:1], v[12:13], 0, v[0:1]
	s_waitcnt vmcnt(3)
	global_store_dwordx4 v[0:1], v[4:7], off nt
	v_lshlrev_b64 v[0:1], 10, v[20:21]
	v_lshl_add_u64 v[0:1], v[12:13], 0, v[0:1]
	s_waitcnt vmcnt(3)
	global_store_dwordx4 v[0:1], v[8:11], off nt
	v_lshlrev_b64 v[0:1], 10, v[22:23]
	v_lshl_add_u64 v[0:1], v[12:13], 0, v[0:1]
	s_waitcnt vmcnt(3)
	global_store_dwordx4 v[0:1], v[24:27], off nt
	v_mov_b32_e32 v0, s7
	ds_read_b32 v1, v0
	s_lshl_b32 s7, s3, 2
	s_add_i32 s7, s2, s7
	v_mov_b32_e32 v4, s7
	s_ashr_i32 s3, s3, 1
	s_waitcnt lgkmcnt(0)
	v_lshlrev_b32_e32 v1, 2, v1
	v_add_u32_e32 v1, s2, v1
	ds_read_b32 v2, v1 offset:2144
	ds_read_b32 v1, v1 offset:2112
	ds_read_b32 v0, v0 offset:1024
	s_waitcnt lgkmcnt(1)
	v_add_u32_e32 v1, v1, v2
	s_waitcnt lgkmcnt(0)
	v_add_u32_e32 v16, v1, v0
	v_lshl_add_u64 v[0:1], v[14:15], 0, s[10:11]
	global_load_dwordx4 v[0:3], v[0:1], off
	ds_read_b32 v5, v4
	s_add_i32 s10, s3, s18
	s_or_b32 s3, s6, 14
	s_ashr_i32 s11, s10, 31
	s_lshl_b32 s7, s3, 2
	s_waitcnt lgkmcnt(0)
	v_lshlrev_b32_e32 v5, 2, v5
	v_add_u32_e32 v5, s2, v5
	ds_read_b32 v6, v5 offset:2144
	ds_read_b32 v5, v5 offset:2112
	ds_read_b32 v4, v4 offset:1024
	s_lshl_b64 s[10:11], s[10:11], 10
	s_add_i32 s7, s2, s7
	v_mov_b32_e32 v8, s7
	s_waitcnt lgkmcnt(1)
	v_add_u32_e32 v5, v5, v6
	s_waitcnt lgkmcnt(0)
	v_add_u32_e32 v18, v5, v4
	v_lshl_add_u64 v[4:5], v[14:15], 0, s[10:11]
	global_load_dwordx4 v[4:7], v[4:5], off
	ds_read_b32 v9, v8
	s_ashr_i32 s3, s3, 1
	s_add_i32 s10, s3, s18
	s_or_b32 s3, s6, 15
	s_ashr_i32 s11, s10, 31
	s_waitcnt lgkmcnt(0)
	v_lshlrev_b32_e32 v9, 2, v9
	v_add_u32_e32 v9, s2, v9
	ds_read_b32 v10, v9 offset:2144
	ds_read_b32 v9, v9 offset:2112
	ds_read_b32 v8, v8 offset:1024
	s_lshl_b32 s7, s3, 2
	s_lshl_b64 s[10:11], s[10:11], 10
	s_add_i32 s7, s2, s7
	s_waitcnt lgkmcnt(1)
	v_add_u32_e32 v9, v9, v10
	s_waitcnt lgkmcnt(0)
	v_add_u32_e32 v20, v9, v8
	v_lshl_add_u64 v[8:9], v[14:15], 0, s[10:11]
	v_mov_b32_e32 v17, s7
	global_load_dwordx4 v[8:11], v[8:9], off
	ds_read_b32 v19, v17
	s_ashr_i32 s3, s3, 1
	s_add_i32 s10, s3, s18
	s_ashr_i32 s11, s10, 31
	s_lshl_b64 s[10:11], s[10:11], 10
	s_waitcnt lgkmcnt(0)
	v_lshlrev_b32_e32 v19, 2, v19
	v_add_u32_e32 v19, s2, v19
	v_lshl_add_u64 v[24:25], v[14:15], 0, s[10:11]
	ds_read_b32 v21, v19 offset:2144
	ds_read_b32 v19, v19 offset:2112
	ds_read_b32 v17, v17 offset:1024
	global_load_dwordx4 v[24:27], v[24:25], off
	s_or_b32 s3, s6, 16
	s_lshl_b32 s7, s3, 2
	s_waitcnt lgkmcnt(1)
	v_add_u32_e32 v19, v19, v21
	s_waitcnt lgkmcnt(0)
	v_add_u32_e32 v22, v19, v17
	v_ashrrev_i32_e32 v17, 31, v16
	v_lshlrev_b64 v[16:17], 10, v[16:17]
	v_lshl_add_u64 v[16:17], v[12:13], 0, v[16:17]
	v_ashrrev_i32_e32 v19, 31, v18
	v_ashrrev_i32_e32 v21, 31, v20
	v_ashrrev_i32_e32 v23, 31, v22
	s_add_i32 s7, s2, s7
	s_ashr_i32 s3, s3, 1
	s_add_i32 s10, s3, s18
	s_or_b32 s3, s6, 17
	s_ashr_i32 s11, s10, 31
	s_lshl_b64 s[10:11], s[10:11], 10
	s_waitcnt vmcnt(3)
	global_store_dwordx4 v[16:17], v[0:3], off nt
	s_nop 1
	v_lshlrev_b64 v[0:1], 10, v[18:19]
	v_lshl_add_u64 v[0:1], v[12:13], 0, v[0:1]
	s_waitcnt vmcnt(3)
	global_store_dwordx4 v[0:1], v[4:7], off nt
	v_lshlrev_b64 v[0:1], 10, v[20:21]
	v_lshl_add_u64 v[0:1], v[12:13], 0, v[0:1]
	s_waitcnt vmcnt(3)
	global_store_dwordx4 v[0:1], v[8:11], off nt
	v_lshlrev_b64 v[0:1], 10, v[22:23]
	v_lshl_add_u64 v[0:1], v[12:13], 0, v[0:1]
	s_waitcnt vmcnt(3)
	global_store_dwordx4 v[0:1], v[24:27], off nt
	v_mov_b32_e32 v0, s7
	ds_read_b32 v1, v0
	s_lshl_b32 s7, s3, 2
	s_add_i32 s7, s2, s7
	v_mov_b32_e32 v4, s7
	s_ashr_i32 s3, s3, 1
	s_waitcnt lgkmcnt(0)
	v_lshlrev_b32_e32 v1, 2, v1
	v_add_u32_e32 v1, s2, v1
	ds_read_b32 v2, v1 offset:2144
	ds_read_b32 v1, v1 offset:2112
	ds_read_b32 v0, v0 offset:1024
	s_waitcnt lgkmcnt(1)
	v_add_u32_e32 v1, v1, v2
	s_waitcnt lgkmcnt(0)
	v_add_u32_e32 v16, v1, v0
	v_lshl_add_u64 v[0:1], v[14:15], 0, s[10:11]
	global_load_dwordx4 v[0:3], v[0:1], off
	ds_read_b32 v5, v4
	s_add_i32 s10, s3, s18
	s_or_b32 s3, s6, 18
	s_ashr_i32 s11, s10, 31
	s_lshl_b32 s7, s3, 2
	s_waitcnt lgkmcnt(0)
	v_lshlrev_b32_e32 v5, 2, v5
	v_add_u32_e32 v5, s2, v5
	ds_read_b32 v6, v5 offset:2144
	ds_read_b32 v5, v5 offset:2112
	ds_read_b32 v4, v4 offset:1024
	s_lshl_b64 s[10:11], s[10:11], 10
	s_add_i32 s7, s2, s7
	v_mov_b32_e32 v8, s7
	s_waitcnt lgkmcnt(1)
	v_add_u32_e32 v5, v5, v6
	s_waitcnt lgkmcnt(0)
	v_add_u32_e32 v18, v5, v4
	v_lshl_add_u64 v[4:5], v[14:15], 0, s[10:11]
	global_load_dwordx4 v[4:7], v[4:5], off
	ds_read_b32 v9, v8
	s_ashr_i32 s3, s3, 1
	s_add_i32 s10, s3, s18
	s_or_b32 s3, s6, 19
	s_ashr_i32 s11, s10, 31
	s_waitcnt lgkmcnt(0)
	v_lshlrev_b32_e32 v9, 2, v9
	v_add_u32_e32 v9, s2, v9
	ds_read_b32 v10, v9 offset:2144
	ds_read_b32 v9, v9 offset:2112
	ds_read_b32 v8, v8 offset:1024
	s_lshl_b32 s7, s3, 2
	s_lshl_b64 s[10:11], s[10:11], 10
	s_add_i32 s7, s2, s7
	s_waitcnt lgkmcnt(1)
	v_add_u32_e32 v9, v9, v10
	s_waitcnt lgkmcnt(0)
	v_add_u32_e32 v20, v9, v8
	v_lshl_add_u64 v[8:9], v[14:15], 0, s[10:11]
	v_mov_b32_e32 v17, s7
	global_load_dwordx4 v[8:11], v[8:9], off
	ds_read_b32 v19, v17
	s_ashr_i32 s3, s3, 1
	s_add_i32 s10, s3, s18
	s_ashr_i32 s11, s10, 31
	s_lshl_b64 s[10:11], s[10:11], 10
	s_waitcnt lgkmcnt(0)
	v_lshlrev_b32_e32 v19, 2, v19
	v_add_u32_e32 v19, s2, v19
	v_lshl_add_u64 v[24:25], v[14:15], 0, s[10:11]
	ds_read_b32 v21, v19 offset:2144
	ds_read_b32 v19, v19 offset:2112
	ds_read_b32 v17, v17 offset:1024
	global_load_dwordx4 v[24:27], v[24:25], off
	s_or_b32 s3, s6, 20
	s_lshl_b32 s7, s3, 2
	s_waitcnt lgkmcnt(1)
	v_add_u32_e32 v19, v19, v21
	s_waitcnt lgkmcnt(0)
	v_add_u32_e32 v22, v19, v17
	v_ashrrev_i32_e32 v17, 31, v16
	v_lshlrev_b64 v[16:17], 10, v[16:17]
	v_lshl_add_u64 v[16:17], v[12:13], 0, v[16:17]
	v_ashrrev_i32_e32 v19, 31, v18
	v_ashrrev_i32_e32 v21, 31, v20
	v_ashrrev_i32_e32 v23, 31, v22
	s_add_i32 s7, s2, s7
	s_ashr_i32 s3, s3, 1
	s_add_i32 s10, s3, s18
	s_or_b32 s3, s6, 21
	s_ashr_i32 s11, s10, 31
	s_lshl_b64 s[10:11], s[10:11], 10
	s_waitcnt vmcnt(3)
	global_store_dwordx4 v[16:17], v[0:3], off nt
	s_nop 1
	v_lshlrev_b64 v[0:1], 10, v[18:19]
	v_lshl_add_u64 v[0:1], v[12:13], 0, v[0:1]
	s_waitcnt vmcnt(3)
	global_store_dwordx4 v[0:1], v[4:7], off nt
	v_lshlrev_b64 v[0:1], 10, v[20:21]
	v_lshl_add_u64 v[0:1], v[12:13], 0, v[0:1]
	s_waitcnt vmcnt(3)
	global_store_dwordx4 v[0:1], v[8:11], off nt
	v_lshlrev_b64 v[0:1], 10, v[22:23]
	v_lshl_add_u64 v[0:1], v[12:13], 0, v[0:1]
	s_waitcnt vmcnt(3)
	global_store_dwordx4 v[0:1], v[24:27], off nt
	v_mov_b32_e32 v0, s7
	ds_read_b32 v1, v0
	s_lshl_b32 s7, s3, 2
	s_add_i32 s7, s2, s7
	v_mov_b32_e32 v4, s7
	s_ashr_i32 s3, s3, 1
	s_waitcnt lgkmcnt(0)
	v_lshlrev_b32_e32 v1, 2, v1
	v_add_u32_e32 v1, s2, v1
	ds_read_b32 v2, v1 offset:2144
	ds_read_b32 v1, v1 offset:2112
	ds_read_b32 v0, v0 offset:1024
	s_waitcnt lgkmcnt(1)
	v_add_u32_e32 v1, v1, v2
	s_waitcnt lgkmcnt(0)
	v_add_u32_e32 v16, v1, v0
	v_lshl_add_u64 v[0:1], v[14:15], 0, s[10:11]
	global_load_dwordx4 v[0:3], v[0:1], off
	ds_read_b32 v5, v4
	s_add_i32 s10, s3, s18
	s_or_b32 s3, s6, 22
	s_ashr_i32 s11, s10, 31
	s_lshl_b32 s7, s3, 2
	s_waitcnt lgkmcnt(0)
	v_lshlrev_b32_e32 v5, 2, v5
	v_add_u32_e32 v5, s2, v5
	ds_read_b32 v6, v5 offset:2144
	ds_read_b32 v5, v5 offset:2112
	ds_read_b32 v4, v4 offset:1024
	s_lshl_b64 s[10:11], s[10:11], 10
	s_add_i32 s7, s2, s7
	v_mov_b32_e32 v8, s7
	s_waitcnt lgkmcnt(1)
	v_add_u32_e32 v5, v5, v6
	s_waitcnt lgkmcnt(0)
	v_add_u32_e32 v18, v5, v4
	v_lshl_add_u64 v[4:5], v[14:15], 0, s[10:11]
	global_load_dwordx4 v[4:7], v[4:5], off
	ds_read_b32 v9, v8
	s_ashr_i32 s3, s3, 1
	s_add_i32 s10, s3, s18
	s_or_b32 s3, s6, 23
	s_ashr_i32 s11, s10, 31
	s_waitcnt lgkmcnt(0)
	v_lshlrev_b32_e32 v9, 2, v9
	v_add_u32_e32 v9, s2, v9
	ds_read_b32 v10, v9 offset:2144
	ds_read_b32 v9, v9 offset:2112
	ds_read_b32 v8, v8 offset:1024
	s_lshl_b32 s7, s3, 2
	s_lshl_b64 s[10:11], s[10:11], 10
	s_add_i32 s7, s2, s7
	s_waitcnt lgkmcnt(1)
	v_add_u32_e32 v9, v9, v10
	s_waitcnt lgkmcnt(0)
	v_add_u32_e32 v20, v9, v8
	v_lshl_add_u64 v[8:9], v[14:15], 0, s[10:11]
	v_mov_b32_e32 v17, s7
	global_load_dwordx4 v[8:11], v[8:9], off
	ds_read_b32 v19, v17
	s_ashr_i32 s3, s3, 1
	s_add_i32 s10, s3, s18
	s_ashr_i32 s11, s10, 31
	s_lshl_b64 s[10:11], s[10:11], 10
	s_waitcnt lgkmcnt(0)
	v_lshlrev_b32_e32 v19, 2, v19
	v_add_u32_e32 v19, s2, v19
	v_lshl_add_u64 v[24:25], v[14:15], 0, s[10:11]
	ds_read_b32 v21, v19 offset:2144
	ds_read_b32 v19, v19 offset:2112
	ds_read_b32 v17, v17 offset:1024
	global_load_dwordx4 v[24:27], v[24:25], off
	s_or_b32 s3, s6, 24
	s_lshl_b32 s7, s3, 2
	s_waitcnt lgkmcnt(1)
	v_add_u32_e32 v19, v19, v21
	s_waitcnt lgkmcnt(0)
	v_add_u32_e32 v22, v19, v17
	v_ashrrev_i32_e32 v17, 31, v16
	v_lshlrev_b64 v[16:17], 10, v[16:17]
	v_lshl_add_u64 v[16:17], v[12:13], 0, v[16:17]
	v_ashrrev_i32_e32 v19, 31, v18
	v_ashrrev_i32_e32 v21, 31, v20
	v_ashrrev_i32_e32 v23, 31, v22
	s_add_i32 s7, s2, s7
	s_ashr_i32 s3, s3, 1
	s_add_i32 s10, s3, s18
	s_or_b32 s3, s6, 25
	s_ashr_i32 s11, s10, 31
	s_lshl_b64 s[10:11], s[10:11], 10
	s_waitcnt vmcnt(3)
	global_store_dwordx4 v[16:17], v[0:3], off nt
	s_nop 1
	v_lshlrev_b64 v[0:1], 10, v[18:19]
	v_lshl_add_u64 v[0:1], v[12:13], 0, v[0:1]
	s_waitcnt vmcnt(3)
	global_store_dwordx4 v[0:1], v[4:7], off nt
	v_lshlrev_b64 v[0:1], 10, v[20:21]
	v_lshl_add_u64 v[0:1], v[12:13], 0, v[0:1]
	s_waitcnt vmcnt(3)
	global_store_dwordx4 v[0:1], v[8:11], off nt
	v_lshlrev_b64 v[0:1], 10, v[22:23]
	v_lshl_add_u64 v[0:1], v[12:13], 0, v[0:1]
	s_waitcnt vmcnt(3)
	global_store_dwordx4 v[0:1], v[24:27], off nt
	v_mov_b32_e32 v0, s7
	ds_read_b32 v1, v0
	s_lshl_b32 s7, s3, 2
	s_add_i32 s7, s2, s7
	v_mov_b32_e32 v4, s7
	s_ashr_i32 s3, s3, 1
	s_waitcnt lgkmcnt(0)
	v_lshlrev_b32_e32 v1, 2, v1
	v_add_u32_e32 v1, s2, v1
	ds_read_b32 v2, v1 offset:2144
	ds_read_b32 v1, v1 offset:2112
	ds_read_b32 v0, v0 offset:1024
	s_waitcnt lgkmcnt(1)
	v_add_u32_e32 v1, v1, v2
	s_waitcnt lgkmcnt(0)
	v_add_u32_e32 v16, v1, v0
	v_lshl_add_u64 v[0:1], v[14:15], 0, s[10:11]
	global_load_dwordx4 v[0:3], v[0:1], off
	ds_read_b32 v5, v4
	s_add_i32 s10, s3, s18
	s_or_b32 s3, s6, 26
	s_ashr_i32 s11, s10, 31
	s_lshl_b32 s7, s3, 2
	s_waitcnt lgkmcnt(0)
	v_lshlrev_b32_e32 v5, 2, v5
	v_add_u32_e32 v5, s2, v5
	ds_read_b32 v6, v5 offset:2144
	ds_read_b32 v5, v5 offset:2112
	ds_read_b32 v4, v4 offset:1024
	s_lshl_b64 s[10:11], s[10:11], 10
	s_add_i32 s7, s2, s7
	v_mov_b32_e32 v8, s7
	s_waitcnt lgkmcnt(1)
	v_add_u32_e32 v5, v5, v6
	s_waitcnt lgkmcnt(0)
	v_add_u32_e32 v18, v5, v4
	v_lshl_add_u64 v[4:5], v[14:15], 0, s[10:11]
	global_load_dwordx4 v[4:7], v[4:5], off
	ds_read_b32 v9, v8
	s_ashr_i32 s3, s3, 1
	s_add_i32 s10, s3, s18
	s_or_b32 s3, s6, 27
	s_ashr_i32 s11, s10, 31
	s_waitcnt lgkmcnt(0)
	v_lshlrev_b32_e32 v9, 2, v9
	v_add_u32_e32 v9, s2, v9
	ds_read_b32 v10, v9 offset:2144
	ds_read_b32 v9, v9 offset:2112
	ds_read_b32 v8, v8 offset:1024
	s_lshl_b32 s7, s3, 2
	s_lshl_b64 s[10:11], s[10:11], 10
	s_add_i32 s7, s2, s7
	s_waitcnt lgkmcnt(1)
	v_add_u32_e32 v9, v9, v10
	s_waitcnt lgkmcnt(0)
	v_add_u32_e32 v20, v9, v8
	v_lshl_add_u64 v[8:9], v[14:15], 0, s[10:11]
	v_mov_b32_e32 v17, s7
	global_load_dwordx4 v[8:11], v[8:9], off
	ds_read_b32 v19, v17
	s_ashr_i32 s3, s3, 1
	s_add_i32 s10, s3, s18
	s_ashr_i32 s11, s10, 31
	s_lshl_b64 s[10:11], s[10:11], 10
	s_waitcnt lgkmcnt(0)
	v_lshlrev_b32_e32 v19, 2, v19
	v_add_u32_e32 v19, s2, v19
	v_lshl_add_u64 v[24:25], v[14:15], 0, s[10:11]
	ds_read_b32 v21, v19 offset:2144
	ds_read_b32 v19, v19 offset:2112
	ds_read_b32 v17, v17 offset:1024
	global_load_dwordx4 v[24:27], v[24:25], off
	s_or_b32 s3, s6, 28
	s_lshl_b32 s7, s3, 2
	s_waitcnt lgkmcnt(1)
	v_add_u32_e32 v19, v19, v21
	s_waitcnt lgkmcnt(0)
	v_add_u32_e32 v22, v19, v17
	v_ashrrev_i32_e32 v17, 31, v16
	v_lshlrev_b64 v[16:17], 10, v[16:17]
	v_lshl_add_u64 v[16:17], v[12:13], 0, v[16:17]
	v_ashrrev_i32_e32 v19, 31, v18
	v_ashrrev_i32_e32 v21, 31, v20
	v_ashrrev_i32_e32 v23, 31, v22
	s_add_i32 s7, s2, s7
	s_ashr_i32 s3, s3, 1
	s_add_i32 s10, s3, s18
	s_or_b32 s3, s6, 29
	s_ashr_i32 s11, s10, 31
	s_lshl_b64 s[10:11], s[10:11], 10
	s_waitcnt vmcnt(3)
	global_store_dwordx4 v[16:17], v[0:3], off nt
	s_nop 1
	v_lshlrev_b64 v[0:1], 10, v[18:19]
	v_lshl_add_u64 v[0:1], v[12:13], 0, v[0:1]
	s_waitcnt vmcnt(3)
	global_store_dwordx4 v[0:1], v[4:7], off nt
	v_lshlrev_b64 v[0:1], 10, v[20:21]
	v_lshl_add_u64 v[0:1], v[12:13], 0, v[0:1]
	s_waitcnt vmcnt(3)
	global_store_dwordx4 v[0:1], v[8:11], off nt
	v_lshlrev_b64 v[0:1], 10, v[22:23]
	v_lshl_add_u64 v[0:1], v[12:13], 0, v[0:1]
	s_waitcnt vmcnt(3)
	global_store_dwordx4 v[0:1], v[24:27], off nt
	v_mov_b32_e32 v0, s7
	ds_read_b32 v1, v0
	s_lshl_b32 s7, s3, 2
	s_add_i32 s7, s2, s7
	v_mov_b32_e32 v4, s7
	s_ashr_i32 s3, s3, 1
	s_waitcnt lgkmcnt(0)
	v_lshlrev_b32_e32 v1, 2, v1
	v_add_u32_e32 v1, s2, v1
	ds_read_b32 v2, v1 offset:2144
	ds_read_b32 v1, v1 offset:2112
	ds_read_b32 v0, v0 offset:1024
	s_waitcnt lgkmcnt(1)
	v_add_u32_e32 v1, v1, v2
	s_waitcnt lgkmcnt(0)
	v_add_u32_e32 v16, v1, v0
	v_lshl_add_u64 v[0:1], v[14:15], 0, s[10:11]
	global_load_dwordx4 v[0:3], v[0:1], off
	ds_read_b32 v5, v4
	s_add_i32 s10, s3, s18
	s_or_b32 s3, s6, 30
	s_ashr_i32 s11, s10, 31
	s_lshl_b32 s7, s3, 2
	s_waitcnt lgkmcnt(0)
	v_lshlrev_b32_e32 v5, 2, v5
	v_add_u32_e32 v5, s2, v5
	ds_read_b32 v6, v5 offset:2144
	ds_read_b32 v5, v5 offset:2112
	ds_read_b32 v4, v4 offset:1024
	s_lshl_b64 s[10:11], s[10:11], 10
	s_add_i32 s7, s2, s7
	v_mov_b32_e32 v8, s7
	s_waitcnt lgkmcnt(1)
	v_add_u32_e32 v5, v5, v6
	s_waitcnt lgkmcnt(0)
	v_add_u32_e32 v18, v5, v4
	v_lshl_add_u64 v[4:5], v[14:15], 0, s[10:11]
	global_load_dwordx4 v[4:7], v[4:5], off
	ds_read_b32 v9, v8
	s_ashr_i32 s3, s3, 1
	s_add_i32 s10, s3, s18
	s_or_b32 s3, s6, 31
	s_ashr_i32 s11, s10, 31
	s_waitcnt lgkmcnt(0)
	v_lshlrev_b32_e32 v9, 2, v9
	v_add_u32_e32 v9, s2, v9
	ds_read_b32 v10, v9 offset:2144
	ds_read_b32 v9, v9 offset:2112
	ds_read_b32 v8, v8 offset:1024
	s_lshl_b32 s6, s3, 2
	s_lshl_b64 s[10:11], s[10:11], 10
	s_add_i32 s6, s2, s6
	s_waitcnt lgkmcnt(1)
	v_add_u32_e32 v9, v9, v10
	s_waitcnt lgkmcnt(0)
	v_add_u32_e32 v20, v9, v8
	v_lshl_add_u64 v[8:9], v[14:15], 0, s[10:11]
	v_mov_b32_e32 v17, s6
	global_load_dwordx4 v[8:11], v[8:9], off
	ds_read_b32 v19, v17
	s_waitcnt lgkmcnt(0)
	v_lshlrev_b32_e32 v19, 2, v19
	v_add_u32_e32 v19, s2, v19
	s_ashr_i32 s2, s3, 1
	s_add_i32 s2, s2, s18
	s_ashr_i32 s3, s2, 31
	s_lshl_b64 s[2:3], s[2:3], 10
	v_lshl_add_u64 v[14:15], v[14:15], 0, s[2:3]
	ds_read_b32 v21, v19 offset:2144
	ds_read_b32 v19, v19 offset:2112
	ds_read_b32 v17, v17 offset:1024
	global_load_dwordx4 v[24:27], v[14:15], off
	v_readlane_b32 s2, v255, 40
	v_readlane_b32 s3, v255, 41
	s_waitcnt lgkmcnt(1)
	v_add_u32_e32 v19, v19, v21
	s_waitcnt lgkmcnt(0)
	v_add_u32_e32 v22, v19, v17
	v_ashrrev_i32_e32 v17, 31, v16
	v_lshlrev_b64 v[14:15], 10, v[16:17]
	v_lshl_add_u64 v[14:15], v[12:13], 0, v[14:15]
	v_ashrrev_i32_e32 v19, 31, v18
	v_ashrrev_i32_e32 v21, 31, v20
	v_ashrrev_i32_e32 v23, 31, v22
	s_and_b64 vcc, exec, s[2:3]
	s_waitcnt vmcnt(3)
	global_store_dwordx4 v[14:15], v[0:3], off nt
	s_nop 1
	v_lshlrev_b64 v[0:1], 10, v[18:19]
	v_lshl_add_u64 v[0:1], v[12:13], 0, v[0:1]
	s_waitcnt vmcnt(3)
	global_store_dwordx4 v[0:1], v[4:7], off nt
	v_lshlrev_b64 v[0:1], 10, v[20:21]
	v_lshl_add_u64 v[0:1], v[12:13], 0, v[0:1]
	s_waitcnt vmcnt(3)
	global_store_dwordx4 v[0:1], v[8:11], off nt
	v_lshlrev_b64 v[0:1], 10, v[22:23]
	v_lshl_add_u64 v[0:1], v[12:13], 0, v[0:1]
	s_waitcnt vmcnt(3)
	global_store_dwordx4 v[0:1], v[24:27], off nt
	s_waitcnt vmcnt(0)
	s_barrier
	s_cbranch_vccnz .LBB0_1515
	v_mbcnt_lo_u32_b32 v0, -1, 0
	v_mbcnt_hi_u32_b32 v0, -1, v0
	s_nop 0
	v_cmp_eq_u32_e32 vcc, 0, v0
	s_and_saveexec_b64 s[18:19], vcc
	s_cbranch_execz .LBB0_1514
	v_readlane_b32 s2, v254, 37
	s_waitcnt vmcnt(0) expcnt(0) lgkmcnt(0)
	s_nop 0
	v_mov_b32_e32 v0, s2
	ds_read_b32 v2, v0
	v_readlane_b32 s2, v254, 38
	s_waitcnt lgkmcnt(0)
	v_cmp_ne_u32_e32 vcc, 0, v2
	v_mov_b32_e32 v0, s2
	ds_read_b32 v0, v0
	s_cbranch_vccnz .LBB0_1478
	v_readlane_b32 s6, v252, 8
	v_readlane_b32 s7, v252, 9
	s_load_dwordx2 s[2:3], s[6:7], 0x0
	s_nop 0
	s_load_dword s6, s[6:7], 0x8
	s_mov_b32 s7, 1
	s_waitcnt lgkmcnt(0)
	s_mul_i32 s2, s3, s2
	s_mul_i32 s6, s2, s6
	s_branch .LBB0_1466
